# baseline (speedup 1.0000x reference)
	.text
	.protected	_Z9fast_mainILb0EEvPKiS1_S1_PKfPKcS3_PfS6_PiPyS6_
	.globl	_Z9fast_mainILb0EEvPKiS1_S1_PKfPKcS3_PfS6_PiPyS6_
	.p2align	8
	.type	_Z9fast_mainILb0EEvPKiS1_S1_PKfPKcS3_PfS6_PiPyS6_,@function

.LBB1_6:
	s_or_saveexec_b64 s[4:5], s[4:5]
	s_load_dwordx4 s[8:11], s[0:1], 0x48
	s_xor_b64 exec, exec, s[4:5]
	s_cbranch_execz .LBB1_8
	v_lshlrev_b32_e32 v18, 7, v64
	v_or_b32_e32 v30, v18, v174
	ds_read_b128 v[2:5], v30 offset:35072
	ds_read_b128 v[6:9], v30 offset:35104
	ds_read_b128 v[10:13], v30 offset:35136
	ds_read_b128 v[14:17], v30 offset:35168
	v_mul_u32_u24_e32 v19, 0xf80, v64
	v_add3_u32 v62, v18, v19, v150
	s_movk_i32 s0, 0x80
	ds_read_b128 v[18:21], v62 offset:8192
	ds_read_b128 v[50:53], v150
	ds_read_b128 v[54:57], v150 offset:4096
	ds_read_b128 v[58:61], v62 offset:16384
	ds_read_b128 v[66:69], v150 offset:1024
	ds_read_b128 v[70:73], v150 offset:5120
	v_cmp_gt_u32_e32 vcc, s0, v0
	ds_read_b128 v[74:77], v62 offset:9216
	s_mov_b32 s0, 0x3e8293ee
	s_waitcnt lgkmcnt(0)
	v_cndmask_b32_e32 v25, v57, v53, vcc
	v_cndmask_b32_e32 v24, v56, v52, vcc
	v_cndmask_b32_e32 v23, v55, v51, vcc
	v_cndmask_b32_e32 v22, v54, v50, vcc
	s_nop 1
	v_mfma_f32_32x32x16_bf16 v[2:17], v[18:21], v[22:25], v[2:17]
	ds_read_b128 v[18:21], v30 offset:35328
	ds_read_b128 v[22:25], v30 offset:35360
	ds_read_b128 v[26:29], v30 offset:35392
	ds_read_b128 v[30:33], v30 offset:35424
	ds_read_b128 v[78:81], v62 offset:17408
	s_waitcnt lgkmcnt(1)
	v_mfma_f32_32x32x16_bf16 v[34:49], v[58:61], v[50:53], v[18:33]
	v_cndmask_b32_e32 v53, v73, v69, vcc
	v_cndmask_b32_e32 v52, v72, v68, vcc
	v_cndmask_b32_e32 v51, v71, v67, vcc
	v_cndmask_b32_e32 v50, v70, v66, vcc
	v_mfma_f32_32x32x16_bf16 v[18:33], v[58:61], v[54:57], v[18:33]
	s_nop 0
	v_mfma_f32_32x32x16_bf16 v[2:17], v[74:77], v[50:53], v[2:17]
	ds_read_b128 v[50:53], v150 offset:2048
	ds_read_b128 v[54:57], v150 offset:6144
	ds_read_b128 v[58:61], v62 offset:10240
	s_waitcnt lgkmcnt(1)
	v_cndmask_b32_e32 v77, v57, v53, vcc
	v_cndmask_b32_e32 v76, v56, v52, vcc
	v_cndmask_b32_e32 v75, v55, v51, vcc
	v_mfma_f32_32x32x16_bf16 v[34:49], v[78:81], v[66:69], v[34:49]
	v_cndmask_b32_e32 v74, v54, v50, vcc
	v_mfma_f32_32x32x16_bf16 v[18:33], v[78:81], v[70:73], v[18:33]
	ds_read_b128 v[66:69], v150 offset:3072
	ds_read_b128 v[70:73], v150 offset:7168
	ds_read_b128 v[78:81], v62 offset:11264
	s_waitcnt lgkmcnt(3)
	v_mfma_f32_32x32x16_bf16 v[2:17], v[58:61], v[74:77], v[2:17]
	ds_read_b128 v[58:61], v62 offset:18432
	ds_read_b128 v[74:77], v62 offset:19456
	s_waitcnt lgkmcnt(1)
	v_mfma_f32_32x32x16_bf16 v[34:49], v[58:61], v[50:53], v[34:49]
	v_cndmask_b32_e32 v53, v73, v69, vcc
	v_cndmask_b32_e32 v52, v72, v68, vcc
	v_cndmask_b32_e32 v51, v71, v67, vcc
	v_cndmask_b32_e32 v50, v70, v66, vcc
	v_mfma_f32_32x32x16_bf16 v[18:33], v[58:61], v[54:57], v[18:33]
	s_nop 0
	v_mfma_f32_32x32x16_bf16 v[2:17], v[78:81], v[50:53], v[2:17]
	s_waitcnt lgkmcnt(0)
	v_mfma_f32_32x32x16_bf16 v[34:49], v[74:77], v[66:69], v[34:49]
	s_nop 9
	v_cvt_pk_bf16_f32 v9, v8, v9
	v_cvt_pk_bf16_f32 v8, v6, v7
	v_cvt_pk_bf16_f32 v7, v4, v5
	v_cvt_pk_bf16_f32 v6, v2, v3
	v_mfma_f32_32x32x16_bf16 v[18:33], v[74:77], v[70:73], v[18:33]
	v_cvt_pk_bf16_f32 v5, v40, v41
	v_cvt_pk_bf16_f32 v4, v38, v39
	v_cvt_pk_bf16_f32 v3, v36, v37
	v_cvt_pk_bf16_f32 v2, v34, v35
	v_cvt_pk_bf16_f32 v36, v14, v15
	v_cvt_pk_bf16_f32 v15, v48, v49
	v_cvt_pk_bf16_f32 v35, v12, v13
	v_mfma_f32_32x32x16_bf16 v[48:63], v[2:5], v[6:9], 0
	v_cvt_pk_bf16_f32 v14, v46, v47
	v_cvt_pk_bf16_f32 v13, v44, v45
	v_cvt_pk_bf16_f32 v12, v42, v43
	s_nop 0
	v_cvt_pk_bf16_f32 v5, v24, v25
	v_cvt_pk_bf16_f32 v4, v22, v23
	v_cvt_pk_bf16_f32 v3, v20, v21
	v_cvt_pk_bf16_f32 v2, v18, v19
	v_cvt_pk_bf16_f32 v37, v16, v17
	v_cvt_pk_bf16_f32 v34, v10, v11
	v_cvt_pk_bf16_f32 v21, v32, v33
	v_cvt_pk_bf16_f32 v20, v30, v31
	v_mfma_f32_32x32x16_bf16 v[48:63], v[12:15], v[34:37], v[48:63]
	v_cvt_pk_bf16_f32 v19, v28, v29
	v_cvt_pk_bf16_f32 v18, v26, v27
	v_mfma_f32_32x32x16_bf16 v[2:17], v[2:5], v[6:9], 0
	s_nop 8
	v_mul_f32_e64 v22, v62, s0
	v_mul_f32_e64 v23, v63, s0
	v_mul_f32_e64 v24, v60, s0
	v_mul_f32_e64 v25, v61, s0
	v_mul_f32_e64 v26, v58, s0
	v_mul_f32_e64 v27, v59, s0
	v_mul_f32_e32 v28, s0, v56
	v_mul_f32_e32 v29, s0, v57
	v_mul_f32_e32 v30, s0, v54
	v_mul_f32_e32 v31, s0, v55
	v_mul_f32_e32 v32, s0, v52
	v_mul_f32_e32 v33, s0, v53
	v_mul_f32_e32 v38, s0, v50
	v_mul_f32_e32 v39, s0, v51
	v_mfma_f32_32x32x16_bf16 v[2:17], v[18:21], v[34:37], v[2:17]
	v_mul_f32_e64 v40, v48, s0
	v_mul_f32_e64 v41, v49, s0
	s_nop 9
	v_mul_f32_e32 v16, s0, v16
	v_mul_f32_e32 v17, s0, v17
	v_mul_f32_e32 v14, s0, v14
	v_mul_f32_e32 v15, s0, v15
	v_mul_f32_e32 v12, s0, v12
	v_mul_f32_e32 v13, s0, v13
	v_mul_f32_e32 v10, s0, v10
	v_mul_f32_e32 v11, s0, v11
	v_mul_f32_e32 v18, s0, v8
	v_mul_f32_e32 v19, s0, v9
	v_mul_f32_e32 v20, s0, v6
	v_mul_f32_e32 v21, s0, v7
	v_mul_f32_e32 v34, s0, v4
	v_mul_f32_e32 v35, s0, v5
	v_mul_f32_e32 v36, s0, v2
	v_mul_f32_e32 v37, s0, v3
	s_mov_b32 s0, 0xff800000
	v_max3_f32 v2, v40, s0, v41
	v_max3_f32 v2, v2, v38, v39
	v_max3_f32 v2, v2, v32, v33
	v_max3_f32 v2, v2, v30, v31
	v_max3_f32 v2, v2, v28, v29
	v_max3_f32 v2, v2, v26, v27
	v_max3_f32 v2, v2, v24, v25
	v_max3_f32 v2, v2, v22, v23
	v_max3_f32 v2, v2, v36, v37
	v_max3_f32 v2, v2, v34, v35
	v_max3_f32 v2, v2, v20, v21
	v_max3_f32 v2, v2, v18, v19
	v_max3_f32 v2, v2, v10, v11
	v_max3_f32 v2, v2, v12, v13
	v_max3_f32 v2, v2, v14, v15
	v_max3_f32 v2, v2, v16, v17
	v_mov_b32_e32 v3, v2
	s_nop 1
	v_permlane32_swap_b32_e32 v2, v3
	v_max_f32_e32 v3, v3, v3
	v_max_f32_e32 v2, v2, v2
	v_max_f32_e32 v42, v2, v3
	v_lshlrev_b32_e32 v3, 6, v0
	v_lshlrev_b32_e32 v2, 14, v64
	v_and_b32_e32 v3, 0x2000, v3
	v_or3_b32 v43, v2, v3, v150
	v_sub_f32_e32 v2, v40, v42
	v_sub_f32_e32 v3, v41, v42
	v_sub_f32_e32 v4, v38, v42
	v_sub_f32_e32 v5, v39, v42
	v_exp_f32_e32 v2, v2
	v_exp_f32_e32 v3, v3
	v_exp_f32_e32 v4, v4
	v_exp_f32_e32 v5, v5
	v_sub_f32_e32 v6, v32, v42
	v_sub_f32_e32 v7, v33, v42
	v_sub_f32_e32 v8, v30, v42
	v_sub_f32_e32 v9, v31, v42
	v_exp_f32_e32 v6, v6
	v_exp_f32_e32 v7, v7
	v_exp_f32_e32 v8, v8
	v_exp_f32_e32 v9, v9
	v_or_b32_e32 v30, 0x18c00, v43
	ds_write_b128 v30, v[2:5]
	v_or_b32_e32 v2, 0x19000, v43
	ds_write_b128 v2, v[6:9]
	v_sub_f32_e32 v2, v28, v42
	v_sub_f32_e32 v3, v29, v42
	v_sub_f32_e32 v4, v26, v42
	v_sub_f32_e32 v5, v27, v42
	v_exp_f32_e32 v2, v2
	v_exp_f32_e32 v3, v3
	v_exp_f32_e32 v4, v4
	v_exp_f32_e32 v5, v5
	v_sub_f32_e32 v6, v24, v42
	v_sub_f32_e32 v7, v25, v42
	v_sub_f32_e32 v8, v22, v42
	v_sub_f32_e32 v9, v23, v42
	v_exp_f32_e32 v6, v6
	v_exp_f32_e32 v7, v7
	v_exp_f32_e32 v8, v8
	v_exp_f32_e32 v9, v9
	v_or_b32_e32 v22, 0x19400, v43
	ds_write_b128 v22, v[2:5]
	v_or_b32_e32 v2, 0x19800, v43
	ds_write_b128 v2, v[6:9]
	v_sub_f32_e32 v2, v36, v42
	v_sub_f32_e32 v3, v37, v42
	v_sub_f32_e32 v4, v34, v42
	v_sub_f32_e32 v5, v35, v42
	v_exp_f32_e32 v2, v2
	v_exp_f32_e32 v3, v3
	v_exp_f32_e32 v4, v4
	v_exp_f32_e32 v5, v5
	v_sub_f32_e32 v6, v20, v42
	v_sub_f32_e32 v7, v21, v42
	v_sub_f32_e32 v8, v18, v42
	v_sub_f32_e32 v9, v19, v42
	v_exp_f32_e32 v6, v6
	v_exp_f32_e32 v7, v7
	v_exp_f32_e32 v8, v8
	v_exp_f32_e32 v9, v9
	v_or_b32_e32 v18, 0x19c00, v43
	ds_write_b128 v18, v[2:5]
	v_add_u32_e32 v2, 0x1a000, v43
	ds_write_b128 v2, v[6:9]
	v_sub_f32_e32 v2, v10, v42
	v_sub_f32_e32 v3, v11, v42
	v_sub_f32_e32 v4, v12, v42
	v_sub_f32_e32 v5, v13, v42
	v_exp_f32_e32 v2, v2
	v_exp_f32_e32 v3, v3
	v_exp_f32_e32 v4, v4
	v_exp_f32_e32 v5, v5
	v_sub_f32_e32 v6, v14, v42
	v_sub_f32_e32 v7, v15, v42
	v_sub_f32_e32 v8, v16, v42
	v_sub_f32_e32 v9, v17, v42
	v_exp_f32_e32 v6, v6
	v_exp_f32_e32 v7, v7
	v_exp_f32_e32 v8, v8
	v_exp_f32_e32 v9, v9
	v_add_u32_e32 v10, 0x1a400, v43
	ds_write_b128 v10, v[2:5]
	v_add_u32_e32 v2, 0x1a800, v43
	ds_write_b128 v2, v[6:9]
	v_mov_b32_e32 v2, v174
.LBB1_8:
	s_or_b64 exec, exec, s[4:5]
	v_add_u32_e32 v10, v172, v2
	v_or_b32_e32 v2, 0x20c00, v150
	v_or_b32_e32 v6, 0x18c00, v150
	s_waitcnt lgkmcnt(0)
	s_barrier
	ds_read_b128 v[18:21], v10 offset:256
	ds_read_b128 v[22:25], v10 offset:288
	ds_read_b128 v[82:85], v10 offset:320
	ds_read_b128 v[86:89], v10 offset:352
	ds_read_b128 v[74:77], v10 offset:384
	ds_read_b128 v[78:81], v10 offset:416
	ds_read_b128 v[2:5], v2
	ds_read_b128 v[6:9], v6
	ds_read_b128 v[66:69], v10 offset:448
	ds_read_b128 v[70:73], v10 offset:480
	v_or_b32_e32 v10, 0x19000, v150
	ds_read_b128 v[10:13], v10
	s_waitcnt lgkmcnt(3)
	v_mul_f32_e32 v26, v8, v20
	v_mul_f32_e32 v27, v9, v21
	v_mul_f32_e32 v28, v6, v18
	v_mul_f32_e32 v29, v7, v19
	v_or_b32_e32 v14, 0x1ac00, v150
	ds_read_b128 v[14:17], v14
	s_waitcnt lgkmcnt(1)
	v_mul_f32_e32 v12, v12, v24
	v_mul_f32_e32 v13, v13, v25
	v_mul_f32_e32 v10, v10, v22
	v_mul_f32_e32 v11, v11, v23
	v_fma_f32 v30, v8, v20, v12
	v_fma_f32 v31, v9, v21, v13
	v_fma_f32 v32, v6, v18, v10
	v_fma_f32 v33, v7, v19, v11
	v_cvt_pk_bf16_f32 v9, v12, v13
	v_cvt_pk_bf16_f32 v7, v26, v27
	v_cvt_pk_bf16_f32 v8, v10, v11
	v_cvt_pk_bf16_f32 v6, v28, v29
	v_or_b32_e32 v10, 0x21000, v150
	ds_read_b128 v[10:13], v10
	v_mfma_f32_32x32x16_bf16 v[34:49], v[2:5], v[6:9], 0
	v_or_b32_e32 v6, 0x1b000, v150
	ds_read_b128 v[6:9], v6
	s_waitcnt lgkmcnt(2)
	v_mul_f32_e64 v26, v16, v20
	v_mul_f32_e64 v27, v17, v21
	v_mul_f32_e32 v50, v14, v18
	v_mul_f32_e32 v51, v15, v19
	v_or_b32_e32 v102, 0x22000, v150
	s_mov_b32 s4, 0x3727c5ac
	s_waitcnt lgkmcnt(0)
	v_mul_f32_e32 v8, v8, v24
	v_mul_f32_e32 v9, v9, v25
	v_mul_f32_e32 v28, v6, v22
	v_mul_f32_e32 v29, v7, v23
	v_or_b32_e32 v6, 0x19400, v150
	v_fma_f32 v90, v16, v20, v8
	v_fma_f32 v91, v17, v21, v9
	v_fma_f32 v92, v14, v18, v28
	v_fma_f32 v93, v15, v19, v29
	ds_read_b128 v[14:17], v6
	v_or_b32_e32 v6, 0x19800, v150
	v_cvt_pk_bf16_f32 v9, v8, v9
	v_cvt_pk_bf16_f32 v7, v26, v27
	v_cvt_pk_bf16_f32 v8, v28, v29
	ds_read_b128 v[26:29], v6
	v_cvt_pk_bf16_f32 v6, v50, v51
	s_waitcnt lgkmcnt(1)
	v_mul_f32_e32 v94, v14, v82
	v_mul_f32_e32 v95, v15, v83
	s_mov_b32 s0, 0x3c800000
	v_mfma_f32_32x32x16_bf16 v[50:65], v[2:5], v[6:9], 0
	v_mul_f32_e64 v2, v16, v84
	v_mul_f32_e64 v3, v17, v85
	s_waitcnt lgkmcnt(0)
	v_mul_f32_e64 v4, v28, v88
	v_mul_f32_e64 v5, v29, v89
	v_mul_f32_e32 v6, v26, v86
	v_mul_f32_e32 v7, v27, v87
	v_fma_f32 v8, v16, v84, v4
	v_fma_f32 v9, v17, v85, v5
	v_cvt_pk_bf16_f32 v3, v2, v3
	v_or_b32_e32 v2, 0x1b400, v150
	v_fma_f32 v14, v14, v82, v6
	v_fma_f32 v15, v15, v83, v7
	v_add_f32_e32 v26, v8, v30
	v_add_f32_e32 v27, v9, v31
	v_cvt_pk_bf16_f32 v5, v4, v5
	v_cvt_pk_bf16_f32 v4, v6, v7
	ds_read_b128 v[6:9], v2
	v_or_b32_e32 v2, 0x1b800, v150
	v_add_f32_e32 v28, v14, v32
	v_add_f32_e32 v29, v15, v33
	ds_read_b128 v[14:17], v2
	v_cvt_pk_bf16_f32 v2, v94, v95
	s_waitcnt lgkmcnt(1)
	v_mul_f32_e32 v30, v6, v82
	v_mul_f32_e32 v31, v7, v83
	v_mov_b64_e32 v[152:153], s[4:5]
	v_mfma_f32_32x32x16_bf16 v[34:49], v[10:13], v[2:5], v[34:49]
	v_mul_f32_e64 v2, v8, v84
	v_mul_f32_e64 v3, v9, v85
	s_waitcnt lgkmcnt(0)
	v_mul_f32_e64 v4, v16, v88
	v_mul_f32_e64 v5, v17, v89
	v_mul_f32_e32 v14, v14, v86
	v_mul_f32_e32 v15, v15, v87
	v_fma_f32 v8, v8, v84, v4
	v_fma_f32 v9, v9, v85, v5
	v_fma_f32 v6, v6, v82, v14
	v_fma_f32 v7, v7, v83, v15
	v_cvt_pk_bf16_f32 v5, v4, v5
	v_cvt_pk_bf16_f32 v3, v2, v3
	v_cvt_pk_bf16_f32 v4, v14, v15
	v_or_b32_e32 v2, 0x21400, v150
	v_or_b32_e32 v14, 0x19c00, v150
	v_add_f32_e32 v32, v8, v90
	v_add_f32_e32 v33, v9, v91
	v_add_f32_e32 v90, v6, v92
	v_add_f32_e32 v91, v7, v93
	ds_read_b128 v[6:9], v2
	ds_read_b128 v[14:17], v14
	v_cvt_pk_bf16_f32 v2, v30, v31
	s_mov_b32 s13, 0
	s_mov_b64 s[6:7], 0
	v_mfma_f32_32x32x16_bf16 v[50:65], v[10:13], v[2:5], v[50:65]
	v_or_b32_e32 v2, 0x1a000, v150
	ds_read_b128 v[2:5], v2
	v_or_b32_e32 v10, 0x1bc00, v150
	ds_read_b128 v[10:13], v10
	s_waitcnt lgkmcnt(2)
	v_mul_f32_e32 v30, v16, v76
	v_mul_f32_e32 v31, v17, v77
	v_mul_f32_e32 v92, v14, v74
	v_mul_f32_e32 v93, v15, v75
	s_waitcnt lgkmcnt(1)
	v_mul_f32_e32 v4, v4, v80
	v_mul_f32_e32 v5, v5, v81
	v_mul_f32_e32 v94, v2, v78
	v_mul_f32_e32 v95, v3, v79
	v_fma_f32 v2, v16, v76, v4
	v_fma_f32 v3, v17, v77, v5
	v_cvt_pk_bf16_f32 v5, v4, v5
	v_add_f32_e32 v96, v2, v26
	v_add_f32_e32 v97, v3, v27
	v_cvt_pk_bf16_f32 v3, v30, v31
	v_cvt_pk_bf16_f32 v4, v94, v95
	v_cvt_pk_bf16_f32 v2, v92, v93
	v_fma_f32 v14, v14, v74, v94
	v_fma_f32 v15, v15, v75, v95
	s_waitcnt lgkmcnt(0)
	v_mul_f32_e32 v30, v10, v74
	v_mul_f32_e32 v31, v11, v75
	v_mfma_f32_32x32x16_bf16 v[34:49], v[6:9], v[2:5], v[34:49]
	v_or_b32_e32 v2, 0x1c000, v150
	ds_read_b128 v[2:5], v2
	v_add_f32_e64 v98, v14, v28
	v_add_f32_e64 v99, v15, v29
	v_or_b32_e32 v14, 0x21800, v150
	ds_read_b128 v[14:17], v14
	v_mul_f32_e32 v26, v12, v76
	v_mul_f32_e32 v27, v13, v77
	s_waitcnt lgkmcnt(1)
	v_mul_f32_e32 v4, v4, v80
	v_mul_f32_e32 v5, v5, v81
	v_mul_f32_e32 v28, v2, v78
	v_mul_f32_e32 v29, v3, v79
	v_fma_f32 v2, v12, v76, v4
	v_fma_f32 v3, v13, v77, v5
	v_fma_f32 v10, v10, v74, v28
	v_fma_f32 v11, v11, v75, v29
	v_add_f32_e32 v32, v2, v32
	v_add_f32_e32 v33, v3, v33
	v_or_b32_e32 v2, 0x1a400, v150
	v_add_f32_e32 v92, v10, v90
	v_add_f32_e32 v93, v11, v91
	ds_read_b128 v[10:13], v2
	v_or_b32_e32 v2, 0x1a800, v150
	v_cvt_pk_bf16_f32 v5, v4, v5
	v_cvt_pk_bf16_f32 v3, v26, v27
	v_cvt_pk_bf16_f32 v4, v28, v29
	ds_read_b128 v[26:29], v2
	v_cvt_pk_bf16_f32 v2, v30, v31
	s_waitcnt lgkmcnt(1)
	v_mul_f32_e32 v30, v10, v66
	v_mul_f32_e32 v31, v11, v67
	v_mfma_f32_32x32x16_bf16 v[50:65], v[6:9], v[2:5], v[50:65]
	v_mul_f32_e64 v2, v12, v68
	v_mul_f32_e64 v3, v13, v69
	s_waitcnt lgkmcnt(0)
	v_mul_f32_e64 v4, v28, v72
	v_mul_f32_e64 v5, v29, v73
	v_mul_f32_e32 v6, v26, v70
	v_mul_f32_e32 v7, v27, v71
	v_fma_f32 v8, v12, v68, v4
	v_fma_f32 v9, v13, v69, v5
	v_cvt_pk_bf16_f32 v3, v2, v3
	v_or_b32_e32 v2, 0x1c400, v150
	v_fma_f32 v10, v10, v66, v6
	v_fma_f32 v11, v11, v67, v7
	v_add_f32_e32 v94, v8, v96
	v_add_f32_e32 v95, v9, v97
	v_cvt_pk_bf16_f32 v5, v4, v5
	v_cvt_pk_bf16_f32 v4, v6, v7
	ds_read_b128 v[6:9], v2
	v_or_b32_e32 v2, 0x1c800, v150
	v_add_f32_e32 v96, v10, v98
	v_add_f32_e32 v97, v11, v99
	ds_read_b128 v[10:13], v2
	v_cvt_pk_bf16_f32 v2, v30, v31
	s_waitcnt lgkmcnt(1)
	v_mul_f32_e32 v30, v6, v66
	v_mul_f32_e32 v31, v7, v67
	v_or_b32_e32 v98, 0x1f000, v150
	v_mfma_f32_32x32x16_bf16 v[34:49], v[14:17], v[2:5], v[34:49]
	s_waitcnt lgkmcnt(0)
	v_mul_f32_e64 v10, v10, v70
	v_mul_f32_e64 v11, v11, v71
	v_mul_f32_e64 v2, v8, v68
	v_mul_f32_e64 v3, v9, v69
	v_mul_f32_e32 v4, v12, v72
	v_mul_f32_e32 v5, v13, v73
	v_fma_f32 v6, v6, v66, v10
	v_fma_f32 v7, v7, v67, v11
	v_fma_f32 v8, v8, v68, v4
	v_fma_f32 v9, v9, v69, v5
	v_add_f32_e32 v92, v6, v92
	v_add_f32_e32 v93, v7, v93
	v_cvt_pk_bf16_f32 v3, v2, v3
	v_or_b32_e32 v2, 0x21c00, v150
	v_or_b32_e32 v6, 0x1cc00, v150
	v_add_f32_e32 v90, v8, v32
	v_add_f32_e32 v91, v9, v33
	v_cvt_pk_bf16_f32 v5, v4, v5
	v_cvt_pk_bf16_f32 v4, v10, v11
	ds_read_b128 v[26:29], v2
	ds_read_b128 v[6:9], v6
	v_cvt_pk_bf16_f32 v2, v30, v31
	ds_read_b128 v[98:101], v98
	ds_read_b128 v[102:105], v102
	v_mfma_f32_32x32x16_bf16 v[50:65], v[14:17], v[2:5], v[50:65]
	v_or_b32_e32 v2, 0x1d000, v150
	ds_read_b128 v[2:5], v2
	v_or_b32_e32 v14, 0x1ec00, v150
	ds_read_b128 v[30:33], v14
	s_waitcnt lgkmcnt(4)
	v_mul_f32_e32 v12, v6, v18
	v_mul_f32_e32 v13, v7, v19
	v_mul_f32_e32 v10, v8, v20
	v_mul_f32_e32 v11, v9, v21
	s_waitcnt lgkmcnt(1)
	v_mul_f32_e32 v14, v2, v22
	v_mul_f32_e32 v15, v3, v23
	v_mul_f32_e32 v22, v98, v22
	v_mul_f32_e32 v23, v99, v23
	v_fma_f32 v112, v6, v18, v14
	v_fma_f32 v113, v7, v19, v15
	s_waitcnt lgkmcnt(0)
	v_mul_f32_e32 v114, v30, v18
	v_mul_f32_e32 v115, v31, v19
	v_fma_f32 v118, v30, v18, v22
	v_fma_f32 v119, v31, v19, v23
	v_or_b32_e32 v18, 0x1d400, v150
	v_mul_f32_e32 v4, v4, v24
	v_mul_f32_e32 v5, v5, v25
	v_mul_f32_e32 v106, v32, v20
	v_mul_f32_e32 v107, v33, v21
	v_mul_f32_e32 v24, v100, v24
	v_mul_f32_e32 v25, v101, v25
	ds_read_b128 v[98:101], v18
	v_or_b32_e32 v18, 0x1d800, v150
	v_cvt_pk_bf16_f32 v19, v106, v107
	ds_read_b128 v[106:109], v18
	v_fma_f32 v110, v8, v20, v4
	v_fma_f32 v111, v9, v21, v5
	v_cvt_pk_bf16_f32 v5, v4, v5
	v_cvt_pk_bf16_f32 v3, v10, v11
	v_cvt_pk_bf16_f32 v4, v14, v15
	s_waitcnt lgkmcnt(0)
	v_mul_f32_e32 v106, v106, v86
	v_mul_f32_e32 v107, v107, v87
	v_cvt_pk_bf16_f32 v2, v12, v13
	v_mul_f32_e32 v120, v98, v82
	v_mul_f32_e32 v121, v99, v83
	v_mul_f32_e32 v108, v108, v88
	v_mul_f32_e32 v109, v109, v89
	v_fma_f32 v98, v98, v82, v106
	v_fma_f32 v99, v99, v83, v107
	v_mfma_f32_32x32x16_bf16 v[2:17], v[26:29], v[2:5], 0
	v_cvt_pk_bf16_f32 v18, v114, v115
	v_mul_f32_e64 v114, v100, v84
	v_mul_f32_e64 v115, v101, v85
	v_fma_f32 v100, v100, v84, v108
	v_fma_f32 v101, v101, v85, v109
	v_add_f32_e32 v124, v98, v112
	v_add_f32_e32 v125, v99, v113
	v_or_b32_e32 v98, 0x1f400, v150
	v_add_f32_e32 v122, v100, v110
	v_add_f32_e32 v123, v101, v111
	v_cvt_pk_bf16_f32 v101, v108, v109
	v_cvt_pk_bf16_f32 v100, v106, v107
	ds_read_b128 v[106:109], v98
	v_or_b32_e32 v98, 0x1f800, v150
	v_fma_f32 v116, v32, v20, v24
	v_fma_f32 v117, v33, v21, v25
	v_cvt_pk_bf16_f32 v21, v24, v25
	v_cvt_pk_bf16_f32 v20, v22, v23
	ds_read_b128 v[110:113], v98
	v_cvt_pk_bf16_f32 v99, v114, v115
	v_mfma_f32_32x32x16_bf16 v[18:33], v[26:29], v[18:21], 0
	v_cvt_pk_bf16_f32 v98, v120, v121
	s_waitcnt lgkmcnt(1)
	v_mul_f32_e64 v114, v106, v82
	v_mul_f32_e64 v115, v107, v83
	s_waitcnt lgkmcnt(0)
	v_mul_f32_e32 v86, v110, v86
	v_mul_f32_e32 v87, v111, v87
	v_mul_f32_e32 v88, v112, v88
	v_mul_f32_e32 v89, v113, v89
	v_fma_f32 v82, v106, v82, v86
	v_fma_f32 v83, v107, v83, v87
	v_mfma_f32_32x32x16_bf16 v[2:17], v[102:105], v[98:101], v[2:17]
	v_mul_f32_e64 v98, v108, v84
	v_mul_f32_e64 v99, v109, v85
	v_fma_f32 v84, v108, v84, v88
	v_fma_f32 v85, v109, v85, v89
	v_add_f32_e64 v108, v82, v118
	v_add_f32_e64 v109, v83, v119
	v_cvt_pk_bf16_f32 v83, v98, v99
	v_or_b32_e32 v82, 0x22400, v150
	v_or_b32_e32 v98, 0x1dc00, v150
	v_add_f32_e32 v106, v84, v116
	v_add_f32_e32 v107, v85, v117
	v_cvt_pk_bf16_f32 v85, v88, v89
	v_cvt_pk_bf16_f32 v84, v86, v87
	ds_read_b128 v[86:89], v82
	ds_read_b128 v[98:101], v98
	v_cvt_pk_bf16_f32 v82, v114, v115
	s_waitcnt lgkmcnt(0)
	v_mul_f32_e32 v110, v100, v76
	v_mul_f32_e32 v111, v101, v77
	v_mfma_f32_32x32x16_bf16 v[18:33], v[102:105], v[82:85], v[18:33]
	v_or_b32_e32 v82, 0x1e000, v150
	ds_read_b128 v[82:85], v82
	v_or_b32_e32 v102, 0x1fc00, v150
	ds_read_b128 v[102:105], v102
	v_mul_f32_e64 v112, v98, v74
	v_mul_f32_e64 v113, v99, v75
	s_waitcnt lgkmcnt(1)
	v_mul_f32_e32 v84, v84, v80
	v_mul_f32_e32 v85, v85, v81
	v_mul_f32_e32 v114, v82, v78
	v_mul_f32_e32 v115, v83, v79
	v_fma_f32 v82, v100, v76, v84
	v_fma_f32 v83, v101, v77, v85
	v_cvt_pk_bf16_f32 v85, v84, v85
	v_add_f32_e32 v116, v82, v122
	v_add_f32_e32 v117, v83, v123
	v_cvt_pk_bf16_f32 v83, v110, v111
	v_cvt_pk_bf16_f32 v84, v114, v115
	v_cvt_pk_bf16_f32 v82, v112, v113
	v_fma_f32 v98, v98, v74, v114
	v_fma_f32 v99, v99, v75, v115
	s_waitcnt lgkmcnt(0)
	v_mul_f32_e32 v112, v102, v74
	v_mul_f32_e32 v113, v103, v75
	v_mfma_f32_32x32x16_bf16 v[2:17], v[86:89], v[82:85], v[2:17]
	v_or_b32_e32 v82, 0x20000, v150
	ds_read_b128 v[82:85], v82
	v_add_f32_e64 v118, v98, v124
	v_add_f32_e64 v119, v99, v125
	v_mul_f32_e64 v110, v104, v76
	v_mul_f32_e64 v111, v105, v77
	v_or_b32_e32 v98, 0x22800, v150
	ds_read_b128 v[98:101], v98
	s_waitcnt lgkmcnt(1)
	v_mul_f32_e32 v78, v82, v78
	v_mul_f32_e32 v79, v83, v79
	v_mul_f32_e32 v80, v84, v80
	v_mul_f32_e32 v81, v85, v81
	v_fma_f32 v74, v102, v74, v78
	v_fma_f32 v75, v103, v75, v79
	v_fma_f32 v76, v104, v76, v80
	v_fma_f32 v77, v105, v77, v81
	v_add_f32_e32 v104, v74, v108
	v_add_f32_e32 v105, v75, v109
	v_or_b32_e32 v74, 0x1e400, v150
	v_add_f32_e32 v102, v76, v106
	v_add_f32_e32 v103, v77, v107
	v_cvt_pk_bf16_f32 v77, v80, v81
	v_cvt_pk_bf16_f32 v76, v78, v79
	ds_read_b128 v[78:81], v74
	v_or_b32_e32 v74, 0x1e800, v150
	ds_read_b128 v[82:85], v74
	v_cvt_pk_bf16_f32 v75, v110, v111
	v_cvt_pk_bf16_f32 v74, v112, v113
	s_waitcnt lgkmcnt(0)
	v_mul_f32_e32 v82, v82, v70
	v_mul_f32_e32 v83, v83, v71
	v_mfma_f32_32x32x16_bf16 v[18:33], v[86:89], v[74:77], v[18:33]
	v_mul_f32_e64 v74, v80, v68
	v_mul_f32_e64 v75, v81, v69
	v_mul_f32_e64 v76, v84, v72
	v_mul_f32_e64 v77, v85, v73
	v_mul_f32_e64 v86, v78, v66
	v_mul_f32_e64 v87, v79, v67
	v_fma_f32 v80, v80, v68, v76
	v_fma_f32 v81, v81, v69, v77
	v_fma_f32 v78, v78, v66, v82
	v_fma_f32 v79, v79, v67, v83
	v_cvt_pk_bf16_f32 v75, v74, v75
	v_or_b32_e32 v74, 0x20400, v150
	v_add_f32_e32 v88, v80, v116
	v_add_f32_e32 v89, v81, v117
	v_add_f32_e32 v106, v78, v118
	v_add_f32_e32 v107, v79, v119
	ds_read_b128 v[78:81], v74
	v_or_b32_e32 v74, 0x20800, v150
	v_cvt_pk_bf16_f32 v77, v76, v77
	v_cvt_pk_bf16_f32 v76, v82, v83
	ds_read_b128 v[82:85], v74
	v_cvt_pk_bf16_f32 v74, v86, v87
	s_waitcnt lgkmcnt(0)
	v_mul_f32_e32 v72, v84, v72
	v_mul_f32_e32 v73, v85, v73
	v_mfma_f32_32x32x16_bf16 v[2:17], v[98:101], v[74:77], v[2:17]
	v_mul_f32_e64 v74, v80, v68
	v_mul_f32_e64 v75, v81, v69
	v_fma_f32 v68, v80, v68, v72
	v_fma_f32 v69, v81, v69, v73
	v_mul_f32_e64 v70, v82, v70
	v_mul_f32_e64 v71, v83, v71
	v_add_f32_e32 v84, v68, v102
	v_add_f32_e32 v85, v69, v103
	v_cvt_pk_bf16_f32 v69, v72, v73
	v_pk_mov_b32 v[72:73], v[96:97], v[94:95] op_sel:[1,0]
	v_mov_b32_e32 v97, v95
	v_add_f32_e32 v72, v72, v96
	v_add_f32_e32 v73, v73, v97
	v_mul_f32_e32 v76, v78, v66
	v_mul_f32_e32 v77, v79, v67
	v_fma_f32 v66, v78, v66, v70
	v_fma_f32 v67, v79, v67, v71
	v_add_f32_e32 v72, v72, v73
	v_mov_b32_e32 v73, v72
	v_add_f32_e32 v86, v66, v104
	v_add_f32_e32 v87, v67, v105
	v_mov_b32_e32 v66, v72
	s_nop 1
	v_permlane32_swap_b32_e32 v72, v66
	v_add_f32_e32 v66, v72, v66
	v_cvt_pk_bf16_f32 v67, v74, v75
	v_rcp_f32_e32 v74, v66
	v_cvt_pk_bf16_f32 v68, v70, v71
	v_cvt_pk_bf16_f32 v66, v76, v77
	v_mul_f32_e32 v70, v46, v74
	v_mul_f32_e32 v71, v47, v74
	s_nop 0
	v_mfma_f32_32x32x16_bf16 v[18:33], v[98:101], v[66:69], v[18:33]
	v_mul_f32_e64 v66, v42, v74
	v_mul_f32_e64 v67, v43, v74
	v_pk_mov_b32 v[42:43], v[92:93], v[90:91] op_sel:[1,0]
	v_mov_b32_e32 v93, v91
	v_add_f32_e32 v42, v42, v92
	v_add_f32_e32 v43, v43, v93
	v_mul_f32_e32 v68, v44, v74
	v_mul_f32_e32 v69, v45, v74
	v_add_f32_e32 v42, v42, v43
	v_mov_b32_e32 v43, v42
	v_pk_mov_b32 v[44:45], v[106:107], v[88:89] op_sel:[1,0]
	v_mov_b32_e32 v43, v42
	s_nop 1
	v_permlane32_swap_b32_e32 v42, v43
	v_add_f32_e32 v42, v42, v43
	v_rcp_f32_e32 v42, v42
	v_mov_b32_e32 v107, v89
	v_add_f32_e32 v44, v44, v106
	v_add_f32_e32 v45, v45, v107
	v_mul_f32_e32 v72, v48, v74
	v_mul_f32_e32 v73, v49, v74
	v_add_f32_e32 v44, v44, v45
	v_mov_b32_e32 v45, v44
	v_mul_f32_e32 v36, v36, v74
	v_mul_f32_e32 v37, v37, v74
	v_mul_f32_e32 v38, v38, v74
	v_mul_f32_e32 v39, v39, v74
	v_mul_f32_e32 v40, v40, v74
	v_mul_f32_e32 v41, v41, v74
	v_mul_f32_e32 v34, v34, v74
	v_mul_f32_e32 v35, v35, v74
	v_mul_f32_e32 v74, v58, v42
	v_mul_f32_e32 v75, v59, v42
	v_mul_f32_e32 v78, v60, v42
	v_mul_f32_e32 v79, v61, v42
	v_mul_f32_e32 v80, v62, v42
	v_mul_f32_e32 v81, v63, v42
	v_mul_f32_e32 v82, v64, v42
	v_mul_f32_e32 v83, v65, v42
	v_mul_f32_e32 v92, v52, v42
	v_mul_f32_e32 v93, v53, v42
	v_mov_b32_e32 v43, v44
	s_nop 1
	v_permlane32_swap_b32_e32 v44, v43
	v_add_f32_e32 v43, v44, v43
	v_rcp_f32_e32 v76, v43
	v_mul_f32_e32 v96, v54, v42
	v_mul_f32_e32 v97, v55, v42
	v_mul_f32_e32 v94, v56, v42
	v_mul_f32_e32 v95, v57, v42
	v_mul_f32_e32 v98, v50, v42
	v_mul_f32_e32 v99, v51, v42
	v_mul_f32_e32 v100, v4, v76
	v_mul_f32_e32 v101, v5, v76
	v_pk_mov_b32 v[4:5], v[86:87], v[84:85] op_sel:[1,0]
	v_mov_b32_e32 v87, v85
	v_add_f32_e32 v4, v4, v86
	v_add_f32_e32 v5, v5, v87
	v_mul_f32_e32 v102, v6, v76
	v_mul_f32_e32 v103, v7, v76
	v_add_f32_e32 v104, v4, v5
	v_mov_b32_e32 v105, v104
	v_cvt_pk_bf16_f32 v7, v40, v41
	ds_read_b128 v[84:87], v150 offset:52224
	ds_read_b128 v[50:53], v150 offset:35840
	ds_read_b128 v[54:57], v150 offset:36864
	ds_read_b128 v[58:61], v150 offset:37888
	ds_read_b128 v[62:65], v150 offset:38912
	v_cvt_pk_bf16_f32 v6, v38, v39
	v_cvt_pk_bf16_f32 v5, v36, v37
	v_cvt_pk_bf16_f32 v4, v34, v35
	ds_read_b128 v[88:91], v150 offset:53248
	ds_read_b128 v[34:37], v150 offset:39936
	ds_read_b128 v[38:41], v150 offset:40960
	ds_read_b128 v[42:45], v150 offset:41984
	ds_read_b128 v[46:49], v150 offset:43008
	v_cvt_pk_bf16_f32 v95, v94, v95
	v_cvt_pk_bf16_f32 v94, v96, v97
	v_cvt_pk_bf16_f32 v93, v92, v93
	v_cvt_pk_bf16_f32 v92, v98, v99
	s_waitcnt lgkmcnt(5)
	v_mfma_f32_32x32x16_bf16 v[50:65], v[84:87], v[4:7], v[50:65]
	v_mul_f32_e64 v10, v10, v76
	v_mul_f32_e64 v11, v11, v76
	v_mul_f32_e64 v12, v12, v76
	v_mul_f32_e64 v13, v13, v76
	v_mul_f32_e64 v8, v8, v76
	v_mul_f32_e64 v9, v9, v76
	v_mov_b32_e32 v77, v104
	s_nop 1
	v_permlane32_swap_b32_e32 v104, v77
	v_cvt_pk_bf16_f32 v73, v72, v73
	s_waitcnt lgkmcnt(0)
	v_mfma_f32_32x32x16_bf16 v[34:49], v[84:87], v[92:95], v[34:49]
	v_cvt_pk_bf16_f32 v72, v70, v71
	v_cvt_pk_bf16_f32 v70, v66, v67
	v_add_f32_e32 v66, v104, v77
	v_cvt_pk_bf16_f32 v71, v68, v69
	v_rcp_f32_e32 v104, v66
	v_cvt_pk_bf16_f32 v69, v82, v83
	v_cvt_pk_bf16_f32 v68, v80, v81
	v_cvt_pk_bf16_f32 v67, v78, v79
	v_cvt_pk_bf16_f32 v66, v74, v75
	ds_read_b128 v[78:81], v150 offset:54272
	v_mfma_f32_32x32x16_bf16 v[50:65], v[88:91], v[70:73], v[50:65]
	v_mul_f32_e64 v2, v2, v76
	v_mul_f32_e64 v3, v3, v76
	v_mul_f32_e64 v20, v20, v104
	v_mul_f32_e64 v21, v21, v104
	v_cvt_pk_bf16_f32 v85, v8, v9
	v_cvt_pk_bf16_f32 v82, v2, v3
	v_mul_f32_e32 v2, v22, v104
	v_mul_f32_e32 v3, v23, v104
	v_mul_f32_e32 v8, v24, v104
	v_mul_f32_e32 v9, v25, v104
	v_mul_f32_e32 v18, v18, v104
	v_mul_f32_e32 v19, v19, v104
	v_mfma_f32_32x32x16_bf16 v[34:49], v[88:91], v[66:69], v[34:49]
	v_cvt_pk_bf16_f32 v84, v102, v103
	v_cvt_pk_bf16_f32 v83, v100, v101
	ds_read_b128 v[86:89], v150 offset:55296
	v_cvt_pk_bf16_f32 v99, v8, v9
	v_cvt_pk_bf16_f32 v98, v2, v3
	v_cvt_pk_bf16_f32 v97, v20, v21
	v_cvt_pk_bf16_f32 v96, v18, v19
	s_waitcnt lgkmcnt(1)
	v_mfma_f32_32x32x16_bf16 v[50:65], v[78:81], v[82:85], v[50:65]
	v_mul_f32_e64 v2, v14, v76
	v_mul_f32_e64 v3, v15, v76
	v_mul_f32_e64 v8, v16, v76
	v_mul_f32_e64 v9, v17, v76
	v_mul_f32_e64 v14, v26, v104
	v_mul_f32_e64 v15, v27, v104
	v_cvt_pk_bf16_f32 v77, v8, v9
	v_cvt_pk_bf16_f32 v76, v2, v3
	v_cvt_pk_bf16_f32 v74, v10, v11
	v_mul_f32_e32 v2, v28, v104
	v_mul_f32_e32 v3, v29, v104
	v_mfma_f32_32x32x16_bf16 v[34:49], v[78:81], v[96:99], v[34:49]
	v_mul_f32_e64 v8, v30, v104
	v_mul_f32_e64 v9, v31, v104
	v_mul_f32_e64 v10, v32, v104
	v_mul_f32_e64 v11, v33, v104
	v_cvt_pk_bf16_f32 v75, v12, v13
	v_cvt_pk_bf16_f32 v81, v10, v11
	v_cvt_pk_bf16_f32 v80, v8, v9
	v_cvt_pk_bf16_f32 v79, v2, v3
	v_cvt_pk_bf16_f32 v78, v14, v15
	s_waitcnt lgkmcnt(0)
	v_mfma_f32_32x32x16_bf16 v[50:65], v[86:89], v[74:77], v[50:65]
	v_mfma_f32_32x32x16_bf16 v[34:49], v[86:89], v[78:81], v[34:49]
	ds_read_b128 v[86:89], v150 offset:56320
	ds_read_b128 v[18:21], v150 offset:44032
	ds_read_b128 v[22:25], v150 offset:45056
	ds_read_b128 v[26:29], v150 offset:46080
	ds_read_b128 v[30:33], v150 offset:47104
	ds_read_b128 v[100:103], v150 offset:57344
	s_waitcnt lgkmcnt(1)
	v_mfma_f32_32x32x16_bf16 v[18:33], v[86:89], v[4:7], v[18:33]
	ds_read_b128 v[2:5], v150 offset:48128
	ds_read_b128 v[6:9], v150 offset:49152
	ds_read_b128 v[10:13], v150 offset:50176
	ds_read_b128 v[14:17], v150 offset:51200
	s_waitcnt lgkmcnt(0)
	v_mfma_f32_32x32x16_bf16 v[2:17], v[86:89], v[92:95], v[2:17]
	v_mfma_f32_32x32x16_bf16 v[18:33], v[100:103], v[70:73], v[18:33]
	v_mfma_f32_32x32x16_bf16 v[2:17], v[100:103], v[66:69], v[2:17]
	ds_read_b128 v[66:69], v150 offset:58368
	ds_read_b128 v[70:73], v150 offset:59392
	s_waitcnt lgkmcnt(1)
	v_mfma_f32_32x32x16_bf16 v[18:33], v[66:69], v[82:85], v[18:33]
	v_mfma_f32_32x32x16_bf16 v[2:17], v[66:69], v[96:99], v[2:17]
	s_waitcnt lgkmcnt(0)
	v_mfma_f32_32x32x16_bf16 v[18:33], v[70:73], v[74:77], v[18:33]
	v_mfma_f32_32x32x16_bf16 v[2:17], v[70:73], v[78:81], v[2:17]
	s_nop 10
	v_mul_f32_e64 v66, v22, v22
	v_mul_f32_e64 v67, v23, v23
	v_mul_f32_e64 v68, v30, v30
	v_mul_f32_e64 v69, v31, v31
	v_mul_f32_e64 v70, v24, v24
	v_mul_f32_e64 v71, v25, v25
	v_mul_f32_e32 v72, v32, v32
	v_mul_f32_e32 v73, v33, v33
	v_mul_f32_e32 v74, v20, v20
	v_mul_f32_e32 v75, v21, v21
	v_mul_f32_e32 v76, v28, v28
	v_mul_f32_e32 v77, v29, v29
	v_mul_f32_e32 v78, v26, v26
	v_mul_f32_e32 v79, v27, v27
	v_mul_f32_e32 v80, v18, v18
	v_mul_f32_e32 v81, v19, v19
	v_fmac_f32_e32 v78, v58, v58
	v_fmac_f32_e32 v79, v59, v59
	v_fmac_f32_e32 v76, v60, v60
	v_fmac_f32_e32 v77, v61, v61
	v_fmac_f32_e32 v74, v52, v52
	v_fmac_f32_e32 v75, v53, v53
	v_fmac_f32_e32 v72, v64, v64
	v_fmac_f32_e32 v73, v65, v65
	v_fmac_f32_e32 v70, v56, v56
	v_fmac_f32_e32 v71, v57, v57
	v_fmac_f32_e32 v68, v62, v62
	v_fmac_f32_e32 v69, v63, v63
	v_fmac_f32_e32 v66, v54, v54
	v_fmac_f32_e32 v67, v55, v55
	v_fmac_f32_e32 v80, v50, v50
	v_fmac_f32_e32 v81, v51, v51
	v_add_f32_e32 v66, v66, v68
	v_add_f32_e32 v67, v67, v69
	v_add_f32_e32 v68, v70, v72
	v_add_f32_e32 v69, v71, v73
	v_add_f32_e32 v70, v74, v76
	v_add_f32_e32 v71, v75, v77
	v_add_f32_e32 v72, v80, v78
	v_add_f32_e32 v73, v81, v79
	v_add_f32_e32 v68, v70, v68
	v_add_f32_e32 v69, v71, v69
	v_add_f32_e32 v66, v72, v66
	v_add_f32_e32 v67, v73, v67
	v_mul_f32_e32 v72, v14, v14
	v_mul_f32_e32 v73, v15, v15
	v_pk_mov_b32 v[70:71], v[66:67], v[68:69] op_sel:[1,0]
	v_mov_b32_e32 v67, v69
	v_add_f32_e32 v66, v70, v66
	v_add_f32_e32 v67, v71, v67
	v_mul_f32_e32 v70, v6, v6
	v_mul_f32_e32 v71, v7, v7
	v_mul_f32_e32 v74, v8, v8
	v_mul_f32_e32 v75, v9, v9
	v_mul_f32_e32 v76, v16, v16
	v_mul_f32_e32 v77, v17, v17
	v_mul_f32_e32 v78, v4, v4
	v_mul_f32_e32 v79, v5, v5
	v_mul_f32_e32 v80, v12, v12
	v_mul_f32_e32 v81, v13, v13
	v_mul_f32_e32 v82, v10, v10
	v_mul_f32_e32 v83, v11, v11
	v_mul_f32_e32 v84, v2, v2
	v_mul_f32_e32 v85, v3, v3
	v_fmac_f32_e32 v82, v42, v42
	v_fmac_f32_e32 v83, v43, v43
	v_fmac_f32_e32 v80, v44, v44
	v_fmac_f32_e32 v81, v45, v45
	v_fmac_f32_e32 v78, v36, v36
	v_fmac_f32_e32 v79, v37, v37
	v_fmac_f32_e32 v76, v48, v48
	v_fmac_f32_e32 v77, v49, v49
	v_fmac_f32_e32 v74, v40, v40
	v_fmac_f32_e32 v75, v41, v41
	v_fmac_f32_e32 v72, v46, v46
	v_fmac_f32_e32 v73, v47, v47
	v_fmac_f32_e32 v70, v38, v38
	v_fmac_f32_e32 v71, v39, v39
	v_fmac_f32_e32 v84, v34, v34
	v_fmac_f32_e32 v85, v35, v35
	v_add_f32_e32 v70, v70, v72
	v_add_f32_e32 v71, v71, v73
	v_add_f32_e32 v72, v74, v76
	v_add_f32_e32 v73, v75, v77
	v_add_f32_e32 v74, v78, v80
	v_add_f32_e32 v75, v79, v81
	v_add_f32_e32 v76, v84, v82
	v_add_f32_e32 v77, v85, v83
	v_add_f32_e32 v72, v74, v72
	v_add_f32_e32 v73, v75, v73
	v_add_f32_e32 v70, v76, v70
	v_add_f32_e32 v71, v77, v71
	v_add_f32_e32 v66, v66, v67
	v_mov_b32_e32 v67, v66
	v_pk_mov_b32 v[74:75], v[70:71], v[72:73] op_sel:[1,0]
	v_mov_b32_e32 v71, v73
	v_add_f32_e32 v70, v74, v70
	v_add_f32_e32 v71, v75, v71
	v_mov_b32_e32 v69, v66
	v_add_f32_e32 v70, v70, v71
	v_mov_b32_e32 v71, v70
	s_nop 0
	v_permlane32_swap_b32_e32 v66, v69
	v_mov_b32_e32 v68, v70
	s_nop 1
	v_permlane32_swap_b32_e32 v70, v68
	v_mov_b32_e32 v71, v66
	v_add_f32_e32 v66, v70, v68
	v_add_f32_e32 v67, v71, v69
	s_nop 0
	v_fma_f32 v66, v66, s0, v152
	v_fma_f32 v67, v67, s0, v152
	s_mov_b32 s1, 0x800000
	v_mul_f32_e32 v68, 0x4b800000, v67
	v_cmp_gt_f32_e32 vcc, s1, v67
	s_nop 1
	v_cndmask_b32_e32 v67, v67, v68, vcc
	v_rsq_f32_e32 v67, v67
	s_nop 0
	v_mul_f32_e32 v68, 0x45800000, v67
	v_cndmask_b32_e32 v68, v67, v68, vcc
	v_mul_f32_e32 v158, v50, v68
	v_mul_f32_e32 v159, v51, v68
	v_mul_f32_e32 v50, v18, v68
	v_mul_f32_e32 v51, v19, v68
	v_mul_f32_e32 v18, 0x4b800000, v66
	v_cmp_gt_f32_e32 vcc, s1, v66
	v_mul_f32_e32 v80, v60, v68
	v_mul_f32_e32 v81, v61, v68
	v_mul_f32_e32 v60, v28, v68
	v_mul_f32_e32 v61, v29, v68
	v_cndmask_b32_e32 v18, v66, v18, vcc
	v_rsq_f32_e32 v18, v18
	v_mul_f32_e32 v78, v58, v68
	v_mul_f32_e32 v79, v59, v68
	v_mul_f32_e32 v160, v52, v68
	v_mul_f32_e32 v161, v53, v68
	v_mul_f32_e32 v82, v54, v68
	v_mul_f32_e32 v83, v55, v68
	v_mul_f32_e32 v19, 0x45800000, v18
	v_cndmask_b32_e32 v28, v18, v19, vcc
	v_mul_f32_e32 v168, v56, v68
	v_mul_f32_e32 v169, v57, v68
	v_mul_f32_e32 v58, v26, v68
	v_mul_f32_e32 v59, v27, v68
	v_mul_f32_e32 v52, v20, v68
	v_mul_f32_e32 v53, v21, v68
	v_mul_f32_e32 v54, v22, v68
	v_mul_f32_e32 v55, v23, v68
	v_mul_f32_e32 v56, v24, v68
	v_mul_f32_e32 v57, v25, v68
	v_mul_f32_e32 v18, v42, v28
	v_mul_f32_e32 v19, v43, v28
	v_mul_f32_e32 v20, v44, v28
	v_mul_f32_e32 v21, v45, v28
	v_mul_f32_e32 v22, v46, v28
	v_mul_f32_e32 v23, v47, v28
	v_mul_f32_e32 v26, v48, v28
	v_mul_f32_e32 v27, v49, v28
	v_mul_f32_e32 v162, v34, v28
	v_mul_f32_e32 v163, v35, v28
	v_mul_f32_e32 v164, v36, v28
	v_mul_f32_e32 v165, v37, v28
	v_mul_f32_e32 v166, v38, v28
	v_mul_f32_e32 v167, v39, v28
	v_mul_f32_e32 v24, v40, v28
	v_mul_f32_e32 v25, v41, v28
	v_mul_f32_e32 v104, v2, v28
	v_mul_f32_e32 v105, v3, v28
	v_mul_f32_e32 v112, v4, v28
	v_mul_f32_e32 v113, v5, v28
	ds_read_b128 v[2:5], v150 offset:60416
	ds_read_b128 v[34:37], v174 offset:32768
	ds_read_b128 v[38:41], v174 offset:32800
	ds_read_b128 v[42:45], v174 offset:32832
	ds_read_b128 v[46:49], v174 offset:32864
	v_cvt_pk_bf16_f32 v129, v168, v169
	v_cvt_pk_bf16_f32 v128, v82, v83
	v_cvt_pk_bf16_f32 v127, v160, v161
	v_cvt_pk_bf16_f32 v126, v158, v159
	v_cvt_pk_bf16_f32 v137, v24, v25
	v_cvt_pk_bf16_f32 v136, v166, v167
	v_cvt_pk_bf16_f32 v135, v164, v165
	s_waitcnt lgkmcnt(0)
	v_mfma_f32_32x32x16_bf16 v[86:101], v[2:5], v[126:129], v[34:49]
	v_cvt_pk_bf16_f32 v134, v162, v163
	v_mul_f32_e64 v84, v62, v68
	v_mul_f32_e64 v85, v63, v68
	v_mul_f32_e64 v170, v64, v68
	v_mul_f32_e64 v171, v65, v68
	v_mul_f32_e32 v62, v30, v68
	v_mul_f32_e32 v63, v31, v68
	v_mul_f32_e32 v64, v32, v68
	v_mul_f32_e32 v65, v33, v68
	v_mul_f32_e32 v116, v6, v28
	v_mul_f32_e32 v117, v7, v28
	v_mul_f32_e32 v154, v8, v28
	v_mul_f32_e32 v155, v9, v28
	v_mfma_f32_32x32x16_bf16 v[34:49], v[2:5], v[134:137], v[34:49]
	ds_read_b128 v[6:9], v150 offset:61440
	ds_read_b128 v[66:69], v174 offset:32896
	ds_read_b128 v[106:109], v150 offset:64512
	v_cvt_pk_bf16_f32 v125, v170, v171
	v_cvt_pk_bf16_f32 v124, v84, v85
	v_cvt_pk_bf16_f32 v123, v80, v81
	v_cvt_pk_bf16_f32 v122, v78, v79
	v_cvt_pk_bf16_f32 v149, v26, v27
	v_cvt_pk_bf16_f32 v148, v22, v23
	v_cvt_pk_bf16_f32 v147, v20, v21
	v_cvt_pk_bf16_f32 v146, v18, v19
	s_waitcnt lgkmcnt(2)
	v_mfma_f32_32x32x16_bf16 v[86:101], v[6:9], v[122:125], v[86:101]
	v_mul_f32_e64 v102, v10, v28
	v_mul_f32_e64 v103, v11, v28
	v_mul_f32_e64 v110, v12, v28
	v_mul_f32_e64 v111, v13, v28
	v_mul_f32_e64 v114, v14, v28
	v_mul_f32_e64 v115, v15, v28
	v_mul_f32_e32 v156, v16, v28
	v_mul_f32_e32 v157, v17, v28
	ds_read_b128 v[176:179], v174 offset:33536
	ds_read_b128 v[180:183], v174 offset:33568
	ds_read_b128 v[184:187], v174 offset:33600
	ds_read_b128 v[28:31], v174 offset:33632
	ds_read_b128 v[188:191], v174 offset:33792
	ds_read_b128 v[192:195], v174 offset:33824
	ds_read_b128 v[196:199], v174 offset:33856
	ds_read_b128 v[200:203], v174 offset:33888
	ds_read_b128 v[204:207], v150 offset:62464
	v_cvt_pk_bf16_f32 v133, v56, v57
	v_mfma_f32_32x32x16_bf16 v[34:49], v[6:9], v[146:149], v[34:49]
	v_cvt_pk_bf16_f32 v132, v54, v55
	v_cvt_pk_bf16_f32 v131, v52, v53
	v_cvt_pk_bf16_f32 v130, v50, v51
	ds_read_b128 v[70:73], v174 offset:33664
	ds_read_b128 v[74:77], v174 offset:33920
	ds_read_b128 v[208:211], v150 offset:63488
	v_cvt_pk_bf16_f32 v145, v154, v155
	v_cvt_pk_bf16_f32 v144, v116, v117
	v_cvt_pk_bf16_f32 v143, v112, v113
	v_cvt_pk_bf16_f32 v142, v104, v105
	s_waitcnt lgkmcnt(3)
	v_mfma_f32_32x32x16_bf16 v[86:101], v[204:207], v[130:133], v[86:101]
	v_cvt_pk_bf16_f32 v121, v64, v65
	v_cvt_pk_bf16_f32 v120, v62, v63
	v_cvt_pk_bf16_f32 v119, v60, v61
	v_cvt_pk_bf16_f32 v118, v58, v59
	v_cvt_pk_bf16_f32 v141, v156, v157
	v_cvt_pk_bf16_f32 v140, v114, v115
	v_cvt_pk_bf16_f32 v139, v110, v111
	v_mfma_f32_32x32x16_bf16 v[34:49], v[204:207], v[142:145], v[34:49]
	v_cvt_pk_bf16_f32 v138, v102, v103
	v_fma_f32 v16, v30, v170, v202
	v_fma_f32 v17, v31, v171, v203
	v_or_b32_e32 v170, 0x12c00, v150
	v_fma_f32 v14, v28, v84, v200
	v_fma_f32 v15, v29, v85, v201
	v_fma_f32 v12, v186, v80, v198
	v_fma_f32 v13, v187, v81, v199
	v_fma_f32 v10, v184, v78, v196
	v_fma_f32 v11, v185, v79, v197
	v_fma_f32 v8, v182, v168, v194
	v_fma_f32 v9, v183, v169, v195
	s_waitcnt lgkmcnt(0)
	v_mfma_f32_32x32x16_bf16 v[86:101], v[208:211], v[118:121], v[86:101]
	v_fma_f32 v6, v180, v82, v192
	v_fma_f32 v7, v181, v83, v193
	ds_read_b128 v[78:81], v174 offset:33760
	ds_read_b128 v[82:85], v174 offset:33248
	v_fma_f32 v4, v178, v160, v190
	v_fma_f32 v5, v179, v161, v191
	v_fma_f32 v2, v176, v158, v188
	v_fma_f32 v3, v177, v159, v189
	v_fma_f32 v32, v30, v26, v202
	v_fma_f32 v33, v31, v27, v203
	v_fma_f32 v30, v28, v22, v200
	v_fma_f32 v31, v29, v23, v201
	v_fma_f32 v28, v186, v20, v198
	v_fma_f32 v29, v187, v21, v199
	v_fma_f32 v26, v184, v18, v196
	v_fma_f32 v27, v185, v19, v197
	v_fma_f32 v24, v182, v24, v194
	v_fma_f32 v25, v183, v25, v195
	v_fma_f32 v22, v180, v166, v192
	v_fma_f32 v23, v181, v167, v193
	v_fma_f32 v20, v178, v164, v190
	v_fma_f32 v21, v179, v165, v191
	v_fma_f32 v18, v176, v162, v188
	v_fma_f32 v19, v177, v163, v189
	ds_read_b128 v[158:161], v174 offset:33696
	ds_read_b128 v[162:165], v174 offset:33728
	ds_read_b128 v[166:169], v174 offset:33952
	ds_read_b128 v[176:179], v174 offset:33984
	ds_read_b128 v[180:183], v174 offset:34016
	ds_read_b128 v[184:187], v170
	v_mfma_f32_32x32x16_bf16 v[34:49], v[208:211], v[138:141], v[34:49]
	v_cvt_pk_bf16_f32 v86, v86, v87
	v_cvt_pk_bf16_f32 v87, v88, v89
	v_cvt_pk_bf16_f32 v88, v90, v91
	v_or_b32_e32 v90, 0x13000, v150
	v_cvt_pk_bf16_f32 v89, v92, v93
	ds_read_b128 v[90:93], v90
	v_pk_max_i16 v86, v86, 0
	v_pk_max_i16 v87, v87, 0
	v_pk_max_i16 v88, v88, 0
	v_pk_max_i16 v89, v89, 0
	s_nop 1
	s_nop 5
	v_cvt_pk_bf16_f32 v188, v34, v35
	v_cvt_pk_bf16_f32 v189, v36, v37
	v_cvt_pk_bf16_f32 v190, v38, v39
	v_cvt_pk_bf16_f32 v191, v40, v41
	v_or_b32_e32 v34, 0x14c00, v150
	s_waitcnt lgkmcnt(1)
	v_mfma_f32_32x32x16_bf16 v[2:17], v[184:187], v[86:89], v[2:17]
	v_pk_max_i16 v188, v188, 0
	v_pk_max_i16 v189, v189, 0
	v_pk_max_i16 v190, v190, 0
	v_pk_max_i16 v191, v191, 0
	s_nop 1
	v_cvt_pk_bf16_f32 v94, v94, v95
	v_cvt_pk_bf16_f32 v95, v96, v97
	v_cvt_pk_bf16_f32 v96, v98, v99
	v_cvt_pk_bf16_f32 v97, v100, v101
	v_cvt_pk_bf16_f32 v98, v42, v43
	v_cvt_pk_bf16_f32 v99, v44, v45
	v_mfma_f32_32x32x16_bf16 v[18:33], v[184:187], v[188:191], v[18:33]
	ds_read_b128 v[184:187], v34
	v_cvt_pk_bf16_f32 v100, v46, v47
	v_cvt_pk_bf16_f32 v101, v48, v49
	v_or_b32_e32 v34, 0x15000, v150
	v_fma_f32 v64, v80, v64, v182
	v_fma_f32 v65, v81, v65, v183
	v_fma_f32 v62, v78, v62, v180
	v_fma_f32 v63, v79, v63, v181
	v_fma_f32 v60, v164, v60, v178
	v_fma_f32 v61, v165, v61, v179
	v_fma_f32 v58, v162, v58, v176
	v_fma_f32 v59, v163, v59, v177
	v_pk_max_i16 v94, v94, 0
	v_pk_max_i16 v95, v95, 0
	v_pk_max_i16 v96, v96, 0
	v_pk_max_i16 v97, v97, 0
	s_nop 1
	v_pk_max_i16 v98, v98, 0
	v_pk_max_i16 v99, v99, 0
	v_pk_max_i16 v100, v100, 0
	v_pk_max_i16 v101, v101, 0
	s_nop 1
	v_fma_f32 v56, v160, v56, v168
	v_fma_f32 v57, v161, v57, v169
	s_waitcnt lgkmcnt(1)
	v_mfma_f32_32x32x16_bf16 v[2:17], v[90:93], v[94:97], v[2:17]
	v_fma_f32 v54, v158, v54, v166
	v_fma_f32 v55, v159, v55, v167
	v_fma_f32 v52, v72, v52, v76
	v_fma_f32 v53, v73, v53, v77
	v_fma_f32 v50, v70, v50, v74
	v_fma_f32 v51, v71, v51, v75
	v_fma_f32 v48, v80, v156, v182
	v_fma_f32 v49, v81, v157, v183
	v_fma_f32 v46, v78, v114, v180
	v_fma_f32 v47, v79, v115, v181
	v_fma_f32 v44, v164, v110, v178
	v_fma_f32 v45, v165, v111, v179
	v_fma_f32 v42, v162, v102, v176
	v_fma_f32 v43, v163, v103, v177
	v_mfma_f32_32x32x16_bf16 v[18:33], v[90:93], v[98:101], v[18:33]
	ds_read_b128 v[90:93], v34
	v_fma_f32 v40, v160, v154, v168
	v_fma_f32 v41, v161, v155, v169
	v_fma_f32 v38, v158, v116, v166
	v_fma_f32 v39, v159, v117, v167
	v_fma_f32 v36, v72, v112, v76
	v_fma_f32 v37, v73, v113, v77
	v_fma_f32 v34, v70, v104, v74
	v_fma_f32 v35, v71, v105, v75
	v_or_b32_e32 v110, 0x10400, v150
	s_waitcnt lgkmcnt(1)
	v_mfma_f32_32x32x16_bf16 v[50:65], v[184:187], v[86:89], v[50:65]
	ds_read_b128 v[70:73], v174 offset:32928
	ds_read_b128 v[74:77], v174 offset:32960
	ds_read_b128 v[78:81], v174 offset:32992
	ds_read_b128 v[86:89], v174 offset:33024
	ds_read_b128 v[110:113], v110
	v_mfma_f32_32x32x16_bf16 v[34:49], v[184:187], v[188:191], v[34:49]
	s_waitcnt lgkmcnt(5)
	v_mfma_f32_32x32x16_bf16 v[50:65], v[90:93], v[94:97], v[50:65]
	v_mfma_f32_32x32x16_bf16 v[34:49], v[90:93], v[98:101], v[34:49]
	s_waitcnt lgkmcnt(2)
	v_mfma_f32_32x32x16_bf16 v[90:105], v[106:109], v[126:129], v[66:81]
	v_mfma_f32_32x32x16_bf16 v[66:81], v[106:109], v[134:137], v[66:81]
	v_or_b32_e32 v106, 0x10000, v150
	ds_read_b128 v[106:109], v106
	s_waitcnt lgkmcnt(0)
	v_mfma_f32_32x32x16_bf16 v[90:105], v[106:109], v[122:125], v[90:105]
	v_mfma_f32_32x32x16_bf16 v[66:81], v[106:109], v[146:149], v[66:81]
	v_or_b32_e32 v106, 0x10800, v150
	ds_read_b128 v[106:109], v106
	v_mfma_f32_32x32x16_bf16 v[90:105], v[110:113], v[130:133], v[90:105]
	v_mfma_f32_32x32x16_bf16 v[66:81], v[110:113], v[142:145], v[66:81]
	v_or_b32_e32 v110, 0x13400, v150
	ds_read_b128 v[110:113], v110
	s_waitcnt lgkmcnt(1)
	v_mfma_f32_32x32x16_bf16 v[90:105], v[106:109], v[118:121], v[90:105]
	v_mfma_f32_32x32x16_bf16 v[66:81], v[106:109], v[138:141], v[66:81]
	s_nop 10
	v_cvt_pk_bf16_f32 v90, v90, v91
	v_cvt_pk_bf16_f32 v91, v92, v93
	v_cvt_pk_bf16_f32 v92, v94, v95
	v_cvt_pk_bf16_f32 v94, v98, v99
	v_or_b32_e32 v98, 0x15400, v150
	v_cvt_pk_bf16_f32 v95, v100, v101
	ds_read_b128 v[98:101], v98
	v_cvt_pk_bf16_f32 v66, v66, v67
	v_cvt_pk_bf16_f32 v67, v68, v69
	v_cvt_pk_bf16_f32 v68, v70, v71
	v_or_b32_e32 v70, 0x13800, v150
	v_cvt_pk_bf16_f32 v93, v96, v97
	v_cvt_pk_bf16_f32 v69, v72, v73
	ds_read_b128 v[70:73], v70
	v_pk_max_i16 v90, v90, 0
	v_pk_max_i16 v91, v91, 0
	v_pk_max_i16 v92, v92, 0
	v_pk_max_i16 v93, v93, 0
	s_nop 1
	v_pk_max_i16 v66, v66, 0
	v_pk_max_i16 v67, v67, 0
	v_pk_max_i16 v68, v68, 0
	v_pk_max_i16 v69, v69, 0
	s_nop 1
	v_cvt_pk_bf16_f32 v96, v102, v103
	s_waitcnt lgkmcnt(2)
	v_mfma_f32_32x32x16_bf16 v[2:17], v[110:113], v[90:93], v[2:17]
	v_cvt_pk_bf16_f32 v97, v104, v105
	v_cvt_pk_bf16_f32 v74, v74, v75
	v_cvt_pk_bf16_f32 v75, v76, v77
	v_cvt_pk_bf16_f32 v76, v78, v79
	v_cvt_pk_bf16_f32 v77, v80, v81
	v_pk_max_i16 v94, v94, 0
	v_pk_max_i16 v95, v95, 0
	v_pk_max_i16 v96, v96, 0
	v_pk_max_i16 v97, v97, 0
	s_nop 1
	v_pk_max_i16 v74, v74, 0
	v_pk_max_i16 v75, v75, 0
	v_pk_max_i16 v76, v76, 0
	v_pk_max_i16 v77, v77, 0
	s_nop 1
	v_mfma_f32_32x32x16_bf16 v[18:33], v[110:113], v[66:69], v[18:33]
	s_waitcnt lgkmcnt(1)
	v_mfma_f32_32x32x16_bf16 v[34:49], v[98:101], v[66:69], v[34:49]
	v_or_b32_e32 v66, 0x15800, v150
	ds_read_b128 v[66:69], v66
	v_mfma_f32_32x32x16_bf16 v[50:65], v[98:101], v[90:93], v[50:65]
	s_waitcnt lgkmcnt(1)
	v_mfma_f32_32x32x16_bf16 v[2:17], v[70:73], v[94:97], v[2:17]
	v_mfma_f32_32x32x16_bf16 v[18:33], v[70:73], v[74:77], v[18:33]
	v_or_b32_e32 v70, 0x10c00, v150
	ds_read_b128 v[78:81], v70
	s_waitcnt lgkmcnt(1)
	v_mfma_f32_32x32x16_bf16 v[50:65], v[66:69], v[94:97], v[50:65]
	ds_read_b128 v[90:93], v174 offset:33056
	ds_read_b128 v[94:97], v174 offset:33088
	ds_read_b128 v[98:101], v174 offset:33120
	ds_read_b128 v[70:73], v174 offset:33152
	v_mfma_f32_32x32x16_bf16 v[34:49], v[66:69], v[74:77], v[34:49]
	v_or_b32_e32 v66, 0x11000, v150
	ds_read_b128 v[66:69], v66
	v_or_b32_e32 v74, 0x11400, v150
	ds_read_b128 v[74:77], v74
	s_waitcnt lgkmcnt(3)
	v_mfma_f32_32x32x16_bf16 v[102:117], v[78:81], v[126:129], v[86:101]
	v_mfma_f32_32x32x16_bf16 v[86:101], v[78:81], v[134:137], v[86:101]
	s_waitcnt lgkmcnt(1)
	v_mfma_f32_32x32x16_bf16 v[86:101], v[66:69], v[146:149], v[86:101]
	v_mfma_f32_32x32x16_bf16 v[102:117], v[66:69], v[122:125], v[102:117]
	v_or_b32_e32 v66, 0x11800, v150
	ds_read_b128 v[66:69], v66
	s_waitcnt lgkmcnt(1)
	v_mfma_f32_32x32x16_bf16 v[86:101], v[74:77], v[142:145], v[86:101]
	v_mfma_f32_32x32x16_bf16 v[102:117], v[74:77], v[130:133], v[102:117]
	v_or_b32_e32 v74, 0x13c00, v150
	ds_read_b128 v[74:77], v74
	s_waitcnt lgkmcnt(1)
	v_mfma_f32_32x32x16_bf16 v[86:101], v[66:69], v[138:141], v[86:101]
	v_mfma_f32_32x32x16_bf16 v[102:117], v[66:69], v[118:121], v[102:117]
	s_nop 10
	v_cvt_pk_bf16_f32 v78, v86, v87
	v_cvt_pk_bf16_f32 v80, v90, v91
	v_or_b32_e32 v86, 0x14000, v150
	v_or_b32_e32 v90, 0x15c00, v150
	v_cvt_pk_bf16_f32 v79, v88, v89
	v_cvt_pk_bf16_f32 v81, v92, v93
	ds_read_b128 v[86:89], v86
	ds_read_b128 v[90:93], v90
	v_cvt_pk_bf16_f32 v66, v102, v103
	v_cvt_pk_bf16_f32 v67, v104, v105
	v_cvt_pk_bf16_f32 v68, v106, v107
	v_cvt_pk_bf16_f32 v69, v108, v109
	v_pk_max_i16 v66, v66, 0
	v_pk_max_i16 v67, v67, 0
	v_pk_max_i16 v68, v68, 0
	v_pk_max_i16 v69, v69, 0
	s_nop 1
	v_pk_max_i16 v78, v78, 0
	v_pk_max_i16 v79, v79, 0
	v_pk_max_i16 v80, v80, 0
	v_pk_max_i16 v81, v81, 0
	s_nop 1
	v_cvt_pk_bf16_f32 v94, v94, v95
	s_waitcnt lgkmcnt(2)
	v_mfma_f32_32x32x16_bf16 v[18:33], v[74:77], v[78:81], v[18:33]
	v_cvt_pk_bf16_f32 v95, v96, v97
	v_cvt_pk_bf16_f32 v96, v98, v99
	v_cvt_pk_bf16_f32 v97, v100, v101
	v_pk_max_i16 v94, v94, 0
	v_pk_max_i16 v95, v95, 0
	v_pk_max_i16 v96, v96, 0
	v_pk_max_i16 v97, v97, 0
	s_nop 1
	v_mfma_f32_32x32x16_bf16 v[2:17], v[74:77], v[66:69], v[2:17]
	v_cvt_pk_bf16_f32 v74, v110, v111
	v_cvt_pk_bf16_f32 v75, v112, v113
	v_cvt_pk_bf16_f32 v76, v114, v115
	v_cvt_pk_bf16_f32 v77, v116, v117
	v_pk_max_i16 v74, v74, 0
	v_pk_max_i16 v75, v75, 0
	v_pk_max_i16 v76, v76, 0
	v_pk_max_i16 v77, v77, 0
	s_nop 1
	s_waitcnt lgkmcnt(0)
	v_mfma_f32_32x32x16_bf16 v[50:65], v[90:93], v[66:69], v[50:65]
	v_or_b32_e32 v66, 0x16000, v150
	ds_read_b128 v[66:69], v66
	v_mfma_f32_32x32x16_bf16 v[34:49], v[90:93], v[78:81], v[34:49]
	v_or_b32_e32 v78, 0x11c00, v150
	ds_read_b128 v[102:105], v78
	v_mfma_f32_32x32x16_bf16 v[2:17], v[86:89], v[74:77], v[2:17]
	s_waitcnt lgkmcnt(1)
	v_mfma_f32_32x32x16_bf16 v[50:65], v[66:69], v[74:77], v[50:65]
	ds_read_b128 v[74:77], v174 offset:33184
	ds_read_b128 v[78:81], v174 offset:33216
	v_mfma_f32_32x32x16_bf16 v[34:49], v[66:69], v[94:97], v[34:49]
	v_or_b32_e32 v66, 0x12000, v150
	ds_read_b128 v[66:69], v66
	v_mfma_f32_32x32x16_bf16 v[18:33], v[86:89], v[94:97], v[18:33]
	s_waitcnt lgkmcnt(1)
	v_mfma_f32_32x32x16_bf16 v[86:101], v[102:105], v[126:129], v[70:85]
	v_mfma_f32_32x32x16_bf16 v[70:85], v[102:105], v[134:137], v[70:85]
	v_or_b32_e32 v102, 0x12400, v150
	ds_read_b128 v[102:105], v102
	v_lshlrev_b32_e32 v135, 2, v1
	v_add_u32_e32 v134, v172, v174
	s_waitcnt lgkmcnt(1)
	v_mfma_f32_32x32x16_bf16 v[86:101], v[66:69], v[122:125], v[86:101]
	v_mfma_f32_32x32x16_bf16 v[70:85], v[66:69], v[146:149], v[70:85]
	v_or_b32_e32 v66, 0x12800, v150
	ds_read_b128 v[66:69], v66
	s_waitcnt lgkmcnt(1)
	v_mfma_f32_32x32x16_bf16 v[86:101], v[102:105], v[130:133], v[86:101]
	v_mfma_f32_32x32x16_bf16 v[70:85], v[102:105], v[142:145], v[70:85]
	v_or_b32_e32 v102, 0x14400, v150
	ds_read_b128 v[102:105], v102
	s_waitcnt lgkmcnt(1)
	v_mfma_f32_32x32x16_bf16 v[86:101], v[66:69], v[118:121], v[86:101]
	v_mfma_f32_32x32x16_bf16 v[70:85], v[66:69], v[138:141], v[70:85]
	s_nop 10
	v_cvt_pk_bf16_f32 v68, v90, v91
	v_or_b32_e32 v90, 0x16400, v150
	v_cvt_pk_bf16_f32 v69, v92, v93
	ds_read_b128 v[90:93], v90
	v_cvt_pk_bf16_f32 v66, v86, v87
	v_cvt_pk_bf16_f32 v67, v88, v89
	v_pk_max_i16 v66, v66, 0
	v_pk_max_i16 v67, v67, 0
	v_pk_max_i16 v68, v68, 0
	v_pk_max_i16 v69, v69, 0
	s_nop 1
	v_cvt_pk_bf16_f32 v70, v70, v71
	v_cvt_pk_bf16_f32 v71, v72, v73
	s_waitcnt lgkmcnt(1)
	v_mfma_f32_32x32x16_bf16 v[2:17], v[102:105], v[66:69], v[2:17]
	v_cvt_pk_bf16_f32 v72, v74, v75
	v_or_b32_e32 v74, 0x14800, v150
	v_cvt_pk_bf16_f32 v73, v76, v77
	ds_read_b128 v[74:77], v74
	v_cvt_pk_bf16_f32 v86, v94, v95
	v_cvt_pk_bf16_f32 v87, v96, v97
	v_cvt_pk_bf16_f32 v88, v98, v99
	s_waitcnt lgkmcnt(1)
	v_mfma_f32_32x32x16_bf16 v[50:65], v[90:93], v[66:69], v[50:65]
	v_or_b32_e32 v66, 0x16800, v150
	ds_read_b128 v[66:69], v66
	v_cvt_pk_bf16_f32 v89, v100, v101
	v_pk_max_i16 v86, v86, 0
	v_pk_max_i16 v87, v87, 0
	v_pk_max_i16 v88, v88, 0
	v_pk_max_i16 v89, v89, 0
	s_nop 1
	v_pk_max_i16 v70, v70, 0
	v_pk_max_i16 v71, v71, 0
	v_pk_max_i16 v72, v72, 0
	v_pk_max_i16 v73, v73, 0
	s_nop 1
	v_cvt_pk_bf16_f32 v78, v78, v79
	v_cvt_pk_bf16_f32 v79, v80, v81
	s_waitcnt lgkmcnt(1)
	v_mfma_f32_32x32x16_bf16 v[2:17], v[74:77], v[86:89], v[2:17]
	v_cvt_pk_bf16_f32 v80, v82, v83
	v_cvt_pk_bf16_f32 v81, v84, v85
	v_pk_max_i16 v78, v78, 0
	v_pk_max_i16 v79, v79, 0
	v_pk_max_i16 v80, v80, 0
	v_pk_max_i16 v81, v81, 0
	s_nop 1
	s_waitcnt lgkmcnt(0)
	v_mfma_f32_32x32x16_bf16 v[50:65], v[66:69], v[86:89], v[50:65]
	v_mfma_f32_32x32x16_bf16 v[34:49], v[90:93], v[70:73], v[34:49]
	s_nop 10
	v_add_f32_e64 v130, v10, v58
	v_add_f32_e64 v131, v11, v59
	v_add_f32_e64 v132, v12, v60
	v_add_f32_e64 v133, v13, v61
	v_add_f32_e64 v138, v4, v52
	v_add_f32_e64 v139, v5, v53
	v_add_f32_e32 v140, v16, v64
	v_add_f32_e32 v141, v17, v65
	v_add_f32_e32 v142, v8, v56
	v_add_f32_e32 v143, v9, v57
	v_add_f32_e32 v144, v14, v62
	v_add_f32_e32 v145, v15, v63
	v_add_f32_e32 v146, v6, v54
	v_add_f32_e32 v147, v7, v55
	v_mfma_f32_32x32x16_bf16 v[18:33], v[102:105], v[70:73], v[18:33]
	ds_read2st64_b32 v[70:71], v135 offset0:133 offset1:134
	v_add_f32_e64 v148, v2, v50
	v_add_f32_e64 v149, v3, v51
	v_add_f32_e64 v144, v146, v144
	v_add_f32_e64 v145, v147, v145
	v_add_f32_e32 v140, v142, v140
	v_add_f32_e32 v141, v143, v141
	v_add_f32_e32 v132, v138, v132
	v_add_f32_e32 v133, v139, v133
	v_add_f32_e32 v130, v148, v130
	v_add_f32_e32 v131, v149, v131
	v_add_f32_e32 v132, v132, v140
	v_add_f32_e32 v133, v133, v141
	v_add_f32_e32 v130, v130, v144
	v_add_f32_e32 v131, v131, v145
	v_mfma_f32_32x32x16_bf16 v[34:49], v[66:69], v[78:81], v[34:49]
	v_pk_mov_b32 v[138:139], v[130:131], v[132:133] op_sel:[1,0]
	v_mov_b32_e32 v131, v133
	s_waitcnt vmcnt(0) lgkmcnt(0)
	v_mul_f32_e32 v66, v175, v70
	v_add_f32_e32 v130, v138, v130
	v_add_f32_e32 v131, v139, v131
	ds_write_b32 v173, v66 offset:512
	v_mul_f32_e32 v66, v175, v71
	v_add_f32_e32 v130, v130, v131
	v_mov_b32_e32 v131, v130
	s_waitcnt lgkmcnt(0)
	ds_read_b128 v[102:105], v174 offset:34560
	ds_read_b128 v[98:101], v174 offset:34592
	ds_read_b128 v[110:113], v174 offset:34624
	ds_read_b128 v[106:109], v174 offset:34656
	ds_read_b128 v[114:117], v174 offset:34688
	ds_read_b128 v[122:125], v174 offset:34720
	ds_read_b128 v[118:121], v174 offset:34752
	ds_read_b128 v[126:129], v174 offset:34784
	v_mov_b32_dpp v66, v66 quad_perm:[1,0,3,2] row_mask:0xf bank_mask:0xf bound_ctrl:1
	v_mov_b32_e32 v131, v130
	v_fmac_f32_e32 v66, v175, v71
	s_nop 0
	v_permlane32_swap_b32_e32 v130, v131
	v_add_f32_dpp v66, v66, v66 quad_perm:[2,3,0,1] row_mask:0xf bank_mask:0xf bound_ctrl:1
	v_add_f32_e32 v130, v130, v131
	v_fmamk_f32 v65, v130, 0xbc800000, v65
	v_add_f32_dpp v66, v66, v66 row_half_mirror row_mask:0xf bank_mask:0xf bound_ctrl:1
	v_fmamk_f32 v64, v130, 0xbc800000, v64
	v_fmamk_f32 v63, v130, 0xbc800000, v63
	v_fmamk_f32 v62, v130, 0xbc800000, v62
	v_fmamk_f32 v61, v130, 0xbc800000, v61
	v_fmamk_f32 v60, v130, 0xbc800000, v60
	v_fmamk_f32 v59, v130, 0xbc800000, v59
	v_fmamk_f32 v58, v130, 0xbc800000, v58
	v_fmamk_f32 v57, v130, 0xbc800000, v57
	v_fmamk_f32 v56, v130, 0xbc800000, v56
	v_fmamk_f32 v55, v130, 0xbc800000, v55
	v_fmamk_f32 v54, v130, 0xbc800000, v54
	v_fmamk_f32 v53, v130, 0xbc800000, v53
	v_fmamk_f32 v52, v130, 0xbc800000, v52
	v_fmamk_f32 v51, v130, 0xbc800000, v51
	v_fmac_f32_e32 v50, 0xbc800000, v130
	v_add_f32_dpp v66, v66, v66 row_ror:8 row_mask:0xf bank_mask:0xf bound_ctrl:1
	v_fmamk_f32 v17, v130, 0xbc800000, v17
	v_fmamk_f32 v16, v130, 0xbc800000, v16
	v_fmamk_f32 v15, v130, 0xbc800000, v15
	v_fmamk_f32 v14, v130, 0xbc800000, v14
	v_fmamk_f32 v13, v130, 0xbc800000, v13
	v_fmamk_f32 v12, v130, 0xbc800000, v12
	v_fmamk_f32 v11, v130, 0xbc800000, v11
	v_fmamk_f32 v10, v130, 0xbc800000, v10
	v_fmamk_f32 v9, v130, 0xbc800000, v9
	v_fmamk_f32 v8, v130, 0xbc800000, v8
	v_fmamk_f32 v7, v130, 0xbc800000, v7
	v_fmamk_f32 v6, v130, 0xbc800000, v6
	v_fmamk_f32 v5, v130, 0xbc800000, v5
	v_fmamk_f32 v4, v130, 0xbc800000, v4
	v_fmamk_f32 v3, v130, 0xbc800000, v3
	v_fmac_f32_e32 v2, 0xbc800000, v130
	v_mul_f32_e32 v130, v54, v54
	v_mul_f32_e32 v131, v55, v55
	v_mul_f32_e32 v132, v62, v62
	v_mul_f32_e32 v133, v63, v63
	v_mul_f32_e32 v138, v50, v50
	v_mul_f32_e32 v139, v51, v51
	v_mul_f32_e32 v140, v58, v58
	v_mul_f32_e32 v141, v59, v59
	v_mul_f32_e32 v142, v56, v56
	v_mul_f32_e32 v143, v57, v57
	v_mul_f32_e32 v144, v64, v64
	v_mul_f32_e32 v145, v65, v65
	v_mul_f32_e32 v146, v52, v52
	v_mul_f32_e32 v147, v53, v53
	v_mul_f32_e32 v148, v60, v60
	v_mul_f32_e32 v149, v61, v61
	v_mov_b32_e32 v67, v66
	v_fmac_f32_e32 v148, v12, v12
	v_fmac_f32_e32 v149, v13, v13
	v_fmac_f32_e32 v146, v4, v4
	v_fmac_f32_e32 v147, v5, v5
	v_fmac_f32_e32 v144, v16, v16
	v_fmac_f32_e32 v145, v17, v17
	v_fmac_f32_e32 v142, v8, v8
	v_fmac_f32_e32 v143, v9, v9
	v_fmac_f32_e32 v140, v10, v10
	v_fmac_f32_e32 v141, v11, v11
	v_fmac_f32_e32 v138, v2, v2
	v_fmac_f32_e32 v139, v3, v3
	v_fmac_f32_e32 v132, v14, v14
	v_fmac_f32_e32 v133, v15, v15
	v_fmac_f32_e32 v130, v6, v6
	v_fmac_f32_e32 v131, v7, v7
	v_permlane16_swap_b32_e32 v66, v67
	v_add_f32_e32 v130, v130, v132
	v_add_f32_e32 v131, v131, v133
	v_add_f32_e32 v132, v138, v140
	v_add_f32_e32 v133, v139, v141
	v_add_f32_e32 v138, v142, v144
	v_add_f32_e32 v139, v143, v145
	v_add_f32_e32 v140, v146, v148
	v_add_f32_e32 v141, v147, v149
	v_mfma_f32_32x32x16_bf16 v[18:33], v[74:77], v[78:81], v[18:33]
	v_add_f32_e32 v136, v66, v67
	ds_read_b128 v[70:73], v134 offset:512
	ds_read_b128 v[66:69], v134 offset:544
	ds_read_b128 v[78:81], v134 offset:576
	ds_read_b128 v[74:77], v134 offset:608
	ds_read_b128 v[82:85], v134 offset:640
	ds_read_b128 v[90:93], v134 offset:672
	ds_read_b128 v[86:89], v134 offset:704
	ds_read_b128 v[94:97], v134 offset:736
	v_add_f32_e32 v138, v140, v138
	v_add_f32_e32 v139, v141, v139
	v_add_f32_e32 v130, v132, v130
	v_add_f32_e32 v131, v133, v131
	s_waitcnt lgkmcnt(8)
	v_mul_f32_e32 v140, v126, v62
	v_mul_f32_e32 v141, v127, v63
	v_pk_mov_b32 v[132:133], v[130:131], v[138:139] op_sel:[1,0]
	v_mov_b32_e32 v131, v139
	v_mul_f32_e32 v138, v122, v54
	v_mul_f32_e32 v139, v123, v55
	v_mul_f32_e32 v142, v114, v50
	v_mul_f32_e32 v143, v115, v51
	v_mul_f32_e32 v144, v118, v58
	v_mul_f32_e32 v145, v119, v59
	v_mul_f32_e32 v146, v124, v56
	v_mul_f32_e32 v147, v125, v57
	v_mul_f32_e32 v148, v128, v64
	v_mul_f32_e32 v149, v129, v65
	v_mul_f32_e32 v154, v116, v52
	v_mul_f32_e32 v155, v117, v53
	v_mul_f32_e32 v156, v120, v60
	v_mul_f32_e32 v157, v121, v61
	v_fmac_f32_e32 v154, v104, v4
	v_fmac_f32_e32 v155, v105, v5
	v_fmac_f32_e32 v156, v112, v12
	v_fmac_f32_e32 v157, v113, v13
	v_fmac_f32_e32 v148, v108, v16
	v_fmac_f32_e32 v149, v109, v17
	v_fmac_f32_e32 v146, v100, v8
	v_fmac_f32_e32 v147, v101, v9
	v_fmac_f32_e32 v144, v110, v10
	v_fmac_f32_e32 v145, v111, v11
	v_fmac_f32_e32 v142, v102, v2
	v_fmac_f32_e32 v143, v103, v3
	v_fmac_f32_e32 v140, v106, v14
	v_fmac_f32_e32 v141, v107, v15
	v_fmac_f32_e32 v138, v98, v6
	v_fmac_f32_e32 v139, v99, v7
	v_add_f32_e32 v130, v132, v130
	v_add_f32_e32 v131, v133, v131
	v_add_f32_e32 v138, v138, v140
	v_add_f32_e32 v139, v139, v141
	v_add_f32_e32 v140, v142, v144
	v_add_f32_e32 v141, v143, v145
	v_add_f32_e32 v142, v146, v148
	v_add_f32_e32 v143, v147, v149
	v_add_f32_e32 v144, v154, v156
	v_add_f32_e32 v145, v155, v157
	v_add_f32_e32 v132, v130, v131
	v_mov_b32_e32 v133, v132
	v_add_f32_e32 v142, v144, v142
	v_add_f32_e32 v143, v145, v143
	v_add_f32_e32 v138, v140, v138
	v_add_f32_e32 v139, v141, v139
	v_add_f32_e32 v133, v142, v143
	v_add_f32_e32 v130, v138, v139
	s_waitcnt lgkmcnt(2)
	v_mul_f32_e32 v138, v90, v54
	v_mul_f32_e32 v139, v91, v55
	s_waitcnt lgkmcnt(0)
	v_mul_f32_e32 v140, v94, v62
	v_mul_f32_e32 v141, v95, v63
	v_mul_f32_e32 v142, v82, v50
	v_mul_f32_e32 v143, v83, v51
	v_mul_f32_e32 v144, v86, v58
	v_mul_f32_e32 v145, v87, v59
	v_mul_f32_e32 v146, v92, v56
	v_mul_f32_e32 v147, v93, v57
	v_mul_f32_e32 v148, v96, v64
	v_mul_f32_e32 v149, v97, v65
	v_mul_f32_e32 v154, v84, v52
	v_mul_f32_e32 v155, v85, v53
	v_mul_f32_e32 v156, v88, v60
	v_mul_f32_e32 v157, v89, v61
	v_add_f32_e32 v130, v130, v133
	v_fmac_f32_e32 v156, v80, v12
	v_fmac_f32_e32 v157, v81, v13
	v_fmac_f32_e32 v154, v72, v4
	v_fmac_f32_e32 v155, v73, v5
	v_fmac_f32_e32 v148, v76, v16
	v_fmac_f32_e32 v149, v77, v17
	v_fmac_f32_e32 v146, v68, v8
	v_fmac_f32_e32 v147, v69, v9
	v_fmac_f32_e32 v144, v78, v10
	v_fmac_f32_e32 v145, v79, v11
	v_fmac_f32_e32 v142, v70, v2
	v_fmac_f32_e32 v143, v71, v3
	v_fmac_f32_e32 v140, v74, v14
	v_fmac_f32_e32 v141, v75, v15
	v_fmac_f32_e32 v138, v66, v6
	v_fmac_f32_e32 v139, v67, v7
	v_mov_b32_e32 v133, v130
	v_add_f32_e32 v138, v138, v140
	v_add_f32_e32 v139, v139, v141
	v_add_f32_e32 v140, v142, v144
	v_add_f32_e32 v141, v143, v145
	v_add_f32_e32 v142, v146, v148
	v_add_f32_e32 v143, v147, v149
	v_add_f32_e32 v144, v154, v156
	v_add_f32_e32 v145, v155, v157
	v_permlane32_swap_b32_e32 v130, v133
	v_add_f32_e32 v142, v144, v142
	v_add_f32_e32 v143, v145, v143
	v_add_f32_e32 v160, v130, v133
	v_add_f32_e32 v138, v140, v138
	v_add_f32_e32 v139, v141, v139
	v_add_f32_e32 v133, v142, v143
	v_add_f32_e32 v140, v26, v42
	v_add_f32_e32 v141, v27, v43
	v_add_f32_e32 v142, v28, v44
	v_add_f32_e32 v143, v29, v45
	v_add_f32_e32 v144, v20, v36
	v_add_f32_e32 v145, v21, v37
	v_add_f32_e32 v146, v32, v48
	v_add_f32_e32 v147, v33, v49
	v_add_f32_e32 v148, v24, v40
	v_add_f32_e32 v149, v25, v41
	v_add_f32_e32 v154, v30, v46
	v_add_f32_e32 v155, v31, v47
	v_add_f32_e32 v156, v22, v38
	v_add_f32_e32 v157, v23, v39
	v_add_f32_e32 v158, v18, v34
	v_add_f32_e32 v159, v19, v35
	v_add_f32_e32 v154, v156, v154
	v_add_f32_e32 v155, v157, v155
	v_add_f32_e32 v146, v148, v146
	v_add_f32_e32 v147, v149, v147
	v_add_f32_e32 v142, v144, v142
	v_add_f32_e32 v143, v145, v143
	v_add_f32_e32 v140, v158, v140
	v_add_f32_e32 v141, v159, v141
	v_add_f32_e32 v142, v142, v146
	v_add_f32_e32 v143, v143, v147
	v_add_f32_e32 v140, v140, v154
	v_add_f32_e32 v141, v141, v155
	v_add_f32_e32 v130, v138, v139
	v_pk_mov_b32 v[144:145], v[140:141], v[142:143] op_sel:[1,0]
	v_mov_b32_e32 v141, v143
	v_add_f32_e32 v140, v144, v140
	v_add_f32_e32 v141, v145, v141
	v_add_f32_e32 v133, v130, v133
	v_add_f32_e32 v140, v140, v141
	v_mov_b32_e32 v141, v140
	v_mov_b32_e32 v131, v132
	v_mov_b32_e32 v130, v140
	s_nop 1
	v_permlane32_swap_b32_e32 v140, v130
	v_add_f32_e32 v130, v140, v130
	v_fmamk_f32 v49, v130, 0xbc800000, v49
	v_fmamk_f32 v48, v130, 0xbc800000, v48
	v_fmamk_f32 v47, v130, 0xbc800000, v47
	v_fmamk_f32 v46, v130, 0xbc800000, v46
	v_fmamk_f32 v45, v130, 0xbc800000, v45
	v_fmamk_f32 v44, v130, 0xbc800000, v44
	v_fmamk_f32 v43, v130, 0xbc800000, v43
	v_fmamk_f32 v42, v130, 0xbc800000, v42
	v_fmamk_f32 v41, v130, 0xbc800000, v41
	v_fmamk_f32 v40, v130, 0xbc800000, v40
	v_fmamk_f32 v39, v130, 0xbc800000, v39
	v_fmamk_f32 v38, v130, 0xbc800000, v38
	v_fmamk_f32 v37, v130, 0xbc800000, v37
	v_fmamk_f32 v36, v130, 0xbc800000, v36
	v_fmamk_f32 v35, v130, 0xbc800000, v35
	v_fmac_f32_e32 v34, 0xbc800000, v130
	v_fmamk_f32 v33, v130, 0xbc800000, v33
	v_fmamk_f32 v32, v130, 0xbc800000, v32
	v_fmamk_f32 v31, v130, 0xbc800000, v31
	v_fmamk_f32 v30, v130, 0xbc800000, v30
	v_fmamk_f32 v29, v130, 0xbc800000, v29
	v_fmamk_f32 v28, v130, 0xbc800000, v28
	v_fmamk_f32 v27, v130, 0xbc800000, v27
	v_fmamk_f32 v26, v130, 0xbc800000, v26
	v_fmamk_f32 v25, v130, 0xbc800000, v25
	v_fmamk_f32 v24, v130, 0xbc800000, v24
	v_fmamk_f32 v23, v130, 0xbc800000, v23
	v_fmamk_f32 v22, v130, 0xbc800000, v22
	v_fmamk_f32 v21, v130, 0xbc800000, v21
	v_fmamk_f32 v20, v130, 0xbc800000, v20
	v_fmamk_f32 v19, v130, 0xbc800000, v19
	v_fmac_f32_e32 v18, 0xbc800000, v130
	v_mul_f32_e32 v140, v38, v38
	v_mul_f32_e32 v141, v39, v39
	v_mul_f32_e32 v142, v46, v46
	v_mul_f32_e32 v143, v47, v47
	v_mul_f32_e32 v144, v34, v34
	v_mul_f32_e32 v145, v35, v35
	v_mul_f32_e32 v146, v42, v42
	v_mul_f32_e32 v147, v43, v43
	v_mul_f32_e32 v148, v40, v40
	v_mul_f32_e32 v149, v41, v41
	v_mul_f32_e32 v154, v48, v48
	v_mul_f32_e32 v155, v49, v49
	v_mul_f32_e32 v156, v36, v36
	v_mul_f32_e32 v157, v37, v37
	v_mul_f32_e32 v158, v44, v44
	v_mul_f32_e32 v159, v45, v45
	v_fmac_f32_e32 v156, v20, v20
	v_fmac_f32_e32 v157, v21, v21
	v_fmac_f32_e32 v158, v28, v28
	v_fmac_f32_e32 v159, v29, v29
	v_fmac_f32_e32 v154, v32, v32
	v_fmac_f32_e32 v155, v33, v33
	v_fmac_f32_e32 v148, v24, v24
	v_fmac_f32_e32 v149, v25, v25
	v_fmac_f32_e32 v146, v26, v26
	v_fmac_f32_e32 v147, v27, v27
	v_fmac_f32_e32 v144, v18, v18
	v_fmac_f32_e32 v145, v19, v19
	v_fmac_f32_e32 v142, v30, v30
	v_fmac_f32_e32 v143, v31, v31
	v_fmac_f32_e32 v140, v22, v22
	v_fmac_f32_e32 v141, v23, v23
	v_permlane32_swap_b32_e32 v132, v131
	v_add_f32_e32 v140, v140, v142
	v_add_f32_e32 v141, v141, v143
	v_add_f32_e32 v142, v144, v146
	v_add_f32_e32 v143, v145, v147
	v_add_f32_e32 v144, v148, v154
	v_add_f32_e32 v145, v149, v155
	v_add_f32_e32 v146, v156, v158
	v_add_f32_e32 v147, v157, v159
	v_add_f32_e32 v140, v142, v140
	v_add_f32_e32 v141, v143, v141
	v_add_f32_e32 v144, v146, v144
	v_add_f32_e32 v145, v147, v145
	v_mul_f32_e32 v122, v122, v38
	v_mul_f32_e32 v123, v123, v39
	v_pk_mov_b32 v[142:143], v[140:141], v[144:145] op_sel:[1,0]
	v_mov_b32_e32 v141, v145
	v_add_f32_e32 v140, v142, v140
	v_add_f32_e32 v141, v143, v141
	v_mul_f32_e32 v126, v126, v46
	v_mul_f32_e32 v127, v127, v47
	v_add_f32_e32 v140, v140, v141
	v_mov_b32_e32 v141, v140
	v_mul_f32_e32 v114, v114, v34
	v_mul_f32_e32 v115, v115, v35
	v_mov_b32_e32 v130, v140
	s_nop 1
	v_permlane32_swap_b32_e32 v140, v130
	v_mov_b32_e32 v141, v132
	v_add_f32_e32 v130, v140, v130
	v_add_f32_e32 v131, v141, v131
	v_mul_f32_e32 v118, v118, v42
	v_mul_f32_e32 v119, v119, v43
	v_fma_f32 v130, v130, s0, v152
	v_fma_f32 v131, v131, s0, v152
	v_mul_f32_e32 v124, v124, v40
	v_mul_f32_e32 v125, v125, v41
	v_mul_f32_e32 v132, 0x4b800000, v131
	v_cmp_gt_f32_e32 vcc, s1, v131
	v_mul_f32_e32 v128, v128, v48
	v_mul_f32_e32 v129, v129, v49
	v_mul_f32_e32 v116, v116, v36
	v_mul_f32_e32 v117, v117, v37
	v_mul_f32_e32 v120, v120, v44
	v_mul_f32_e32 v121, v121, v45
	v_cndmask_b32_e32 v131, v131, v132, vcc
	v_mul_f32_e32 v132, 0x4b800000, v130
	v_cmp_gt_f32_e64 s[0:1], s1, v130
	v_fma_f32 v112, v112, v28, v120
	v_fma_f32 v113, v113, v29, v121
	v_fma_f32 v104, v104, v20, v116
	v_fma_f32 v105, v105, v21, v117
	v_fma_f32 v108, v108, v32, v128
	v_fma_f32 v109, v109, v33, v129
	v_fma_f32 v100, v100, v24, v124
	v_fma_f32 v101, v101, v25, v125
	v_fma_f32 v110, v110, v26, v118
	v_fma_f32 v111, v111, v27, v119
	v_fma_f32 v102, v102, v18, v114
	v_fma_f32 v103, v103, v19, v115
	v_fma_f32 v106, v106, v30, v126
	v_fma_f32 v107, v107, v31, v127
	v_fma_f32 v98, v98, v22, v122
	v_fma_f32 v99, v99, v23, v123
	v_rsq_f32_e32 v131, v131
	v_cndmask_b32_e64 v130, v130, v132, s[0:1]
	v_add_f32_e32 v98, v98, v106
	v_add_f32_e32 v99, v99, v107
	v_add_f32_e32 v102, v102, v110
	v_add_f32_e32 v103, v103, v111
	v_add_f32_e32 v100, v100, v108
	v_add_f32_e32 v101, v101, v109
	v_add_f32_e32 v104, v104, v112
	v_add_f32_e32 v105, v105, v113
	v_rsq_f32_e32 v132, v130
	v_add_f32_e32 v100, v104, v100
	v_add_f32_e32 v101, v105, v101
	v_add_f32_e32 v98, v102, v98
	v_add_f32_e32 v99, v103, v99
	v_mul_f32_e32 v130, 0x45800000, v131
	v_add_f32_e32 v98, v98, v99
	v_add_f32_e32 v99, v100, v101
	v_add_f32_e32 v98, v98, v99
	v_mov_b32_e32 v99, v98
	v_mul_f32_e32 v90, v90, v38
	v_mul_f32_e32 v91, v91, v39
	v_mul_f32_e32 v94, v94, v46
	v_mul_f32_e32 v95, v95, v47
	v_mul_f32_e32 v82, v82, v34
	v_mul_f32_e32 v83, v83, v35
	v_mul_f32_e32 v86, v86, v42
	v_mul_f32_e32 v87, v87, v43
	v_cndmask_b32_e32 v130, v131, v130, vcc
	v_mul_f32_e32 v131, 0x45800000, v132
	v_permlane32_swap_b32_e32 v98, v99
	v_fma_f32 v78, v78, v26, v86
	v_fma_f32 v79, v79, v27, v87
	v_fma_f32 v70, v70, v18, v82
	v_fma_f32 v71, v71, v19, v83
	v_fma_f32 v74, v74, v30, v94
	v_fma_f32 v75, v75, v31, v95
	v_fma_f32 v66, v66, v22, v90
	v_fma_f32 v67, v67, v23, v91
	v_cndmask_b32_e64 v131, v132, v131, s[0:1]
	v_add_f32_e32 v98, v98, v99
	v_add_f32_e32 v66, v66, v74
	v_add_f32_e32 v67, v67, v75
	v_add_f32_e32 v70, v70, v78
	v_add_f32_e32 v71, v71, v79
	v_mul_f32_e32 v139, v160, v130
	v_mul_f32_e32 v98, v98, v131
	v_add_f32_e32 v66, v70, v66
	v_add_f32_e32 v67, v71, v67
	v_cmp_gt_u32_e32 vcc, 32, v1
	v_add_f32_e32 v66, v66, v67
	v_mul_f32_e32 v92, v92, v40
	v_mul_f32_e32 v93, v93, v41
	v_cndmask_b32_e32 v67, v98, v139, vcc
	v_add_f32_e32 v67, s12, v67
	v_mul_f32_e32 v96, v96, v48
	v_mul_f32_e32 v97, v97, v49
	v_mul_f32_e32 v84, v84, v36
	v_mul_f32_e32 v85, v85, v37
	v_mul_f32_e32 v88, v88, v44
	v_mul_f32_e32 v89, v89, v45
	v_mul_f32_e32 v67, 0xbfb8aa3b, v67
	v_fma_f32 v80, v80, v28, v88
	v_fma_f32 v81, v81, v29, v89
	v_fma_f32 v72, v72, v20, v84
	v_fma_f32 v73, v73, v21, v85
	v_fma_f32 v76, v76, v32, v96
	v_fma_f32 v77, v77, v33, v97
	v_fma_f32 v68, v68, v24, v92
	v_fma_f32 v69, v69, v25, v93
	v_exp_f32_e32 v70, v67
	v_add_f32_e32 v68, v68, v76
	v_add_f32_e32 v69, v69, v77
	v_add_f32_e32 v72, v72, v80
	v_add_f32_e32 v73, v73, v81
	v_cmp_lt_i32_e64 s[0:1], 0, v151
	v_add_f32_e32 v68, v72, v68
	v_add_f32_e32 v69, v73, v69
	v_mov_b32_e32 v137, v136
	v_add_f32_e32 v67, v68, v69
	v_add_f32_e32 v67, v66, v67
	v_add_f32_e32 v66, 1.0, v70
	v_rcp_f32_e32 v66, v66
	v_mov_b32_e32 v69, 0xff800000
	v_mov_b32_e32 v138, v133
	v_mov_b32_e32 v68, v67
	v_cndmask_b32_e64 v70, v69, v66, s[0:1]
	v_mbcnt_lo_u32_b32 v66, -1, 0
	v_mbcnt_hi_u32_b32 v66, -1, v66
	v_permlane32_swap_b32_e32 v136, v137
	v_permlane32_swap_b32_e32 v133, v138
	v_permlane32_swap_b32_e32 v67, v68
	v_and_b32_e32 v86, 64, v66
	v_mov_b32_e32 v71, 8
	v_mov_b32_e32 v66, 0
.LBB1_9:
	v_mov_b32_dpp v72, v70 quad_perm:[1,0,3,2] row_mask:0xf bank_mask:0xf bound_ctrl:1
	v_max_f32_e32 v73, v70, v70
	v_max_f32_e32 v72, v72, v72
	v_max_f32_e32 v72, v73, v72
	s_nop 1
	v_mov_b32_dpp v73, v72 quad_perm:[2,3,0,1] row_mask:0xf bank_mask:0xf bound_ctrl:1
	v_max_f32_e32 v73, v73, v73
	v_max_f32_e32 v72, v72, v73
	s_nop 1
	v_mov_b32_dpp v73, v72 row_half_mirror row_mask:0xf bank_mask:0xf bound_ctrl:1
	v_max_f32_e32 v73, v73, v73
	v_max_f32_e32 v72, v72, v73
	s_nop 1
	v_mov_b32_dpp v73, v72 row_ror:8 row_mask:0xf bank_mask:0xf bound_ctrl:1
	v_max_f32_e32 v73, v73, v73
	v_max_f32_e32 v72, v72, v73
	v_mov_b32_e32 v73, v72
	s_nop 1
	v_permlane16_swap_b32_e32 v72, v73
	v_max_f32_e32 v73, v73, v73
	v_max_f32_e32 v72, v72, v72
	v_max_f32_e32 v72, v72, v73
	v_mov_b32_e32 v73, v72
	s_nop 1
	v_permlane32_swap_b32_e32 v72, v73
	v_max_f32_e32 v73, v73, v73
	v_max_f32_e32 v72, v72, v72
	v_max_f32_e32 v72, v72, v73
	v_cmp_eq_f32_e64 s[0:1], v70, v72
	s_ff1_i32_b64 s4, s[0:1]
	s_cmp_lg_u64 s[0:1], 0
	s_cselect_b32 s0, s4, -1
	v_and_or_b32 v72, s0, 63, v86
	v_lshlrev_b32_e32 v72, 2, v72
	ds_bpermute_b32 v72, v72, v151
	s_add_i32 s1, s13, 1
	s_cmp_gt_u32 s13, 6
	s_cselect_b64 s[14:15], -1, 0
	s_mov_b32 s13, s1
	s_waitcnt lgkmcnt(0)
	v_min_i32_e32 v72, v72, v71
	v_sub_u32_e32 v71, v71, v72
	v_cmp_gt_i32_e64 s[4:5], 1, v71
	s_or_b64 s[4:5], s[14:15], s[4:5]
	v_cmp_eq_u32_e64 s[0:1], s0, v1
	s_and_b64 s[4:5], exec, s[4:5]
	s_or_b64 s[6:7], s[4:5], s[6:7]
	v_cndmask_b32_e64 v66, v66, v72, s[0:1]
	v_cndmask_b32_e64 v70, v70, v69, s[0:1]
	s_andn2_b64 exec, exec, s[6:7]
	s_cbranch_execnz .LBB1_9
	s_or_b64 exec, exec, s[6:7]
	v_add_f32_e32 v69, v133, v138
	v_add_f32_e32 v67, v67, v68
	v_mul_f32_e32 v69, v69, v130
	v_mul_f32_e32 v67, v67, v131
	v_add_f32_e32 v68, v136, v137
	v_cndmask_b32_e32 v67, v67, v69, vcc
	v_add_f32_e32 v67, v68, v67
	v_mul_f32_e32 v68, 0x3e000000, v67
	v_mov_b32_e32 v69, 0xff800000
	v_cmp_lt_i32_e64 s[0:1], 0, v66
	s_mov_b32 s4, 0x3e000000
	v_cvt_f32_u32_e32 v66, v66
	v_cndmask_b32_e64 v68, v69, v68, s[0:1]
	v_cvt_pk_bf16_f32 v9, v8, v9
	v_cvt_pk_bf16_f32 v8, v6, v7
	v_mov_b32_dpp v69, v68 quad_perm:[1,0,3,2] row_mask:0xf bank_mask:0xf bound_ctrl:1
	v_max_f32_e32 v69, v69, v69
	v_max_f32_e32 v68, v68, v69
	v_cvt_pk_bf16_f32 v6, v2, v3
	v_or_b32_e32 v2, 0x17000, v150
	v_mov_b32_dpp v69, v68 quad_perm:[2,3,0,1] row_mask:0xf bank_mask:0xf bound_ctrl:1
	v_max_f32_e32 v69, v69, v69
	v_max_f32_e32 v68, v68, v69
	v_cvt_pk_bf16_f32 v7, v4, v5
	v_or_b32_e32 v100, 0x18000, v150
	v_mov_b32_dpp v69, v68 row_half_mirror row_mask:0xf bank_mask:0xf bound_ctrl:1
	v_max_f32_e32 v69, v69, v69
	v_max_f32_e32 v68, v68, v69
	v_cvt_pk_bf16_f32 v91, v16, v17
	v_cvt_pk_bf16_f32 v90, v14, v15
	v_mov_b32_dpp v69, v68 row_ror:8 row_mask:0xf bank_mask:0xf bound_ctrl:1
	v_max_f32_e32 v69, v69, v69
	v_max_f32_e32 v68, v68, v69
	v_mov_b32_e32 v69, v68
	s_nop 1
	v_permlane16_swap_b32_e32 v68, v69
	v_max_f32_e32 v69, v69, v69
	v_max_f32_e32 v68, v68, v68
	v_max_f32_e32 v68, v68, v69
	v_mov_b32_e32 v69, v68
	s_nop 1
	v_permlane32_swap_b32_e32 v68, v69
	v_max_f32_e32 v69, v69, v69
	v_max_f32_e32 v68, v68, v68
	v_max_f32_e32 v68, v68, v69
	v_fma_f32 v67, v67, s4, -v68
	v_mul_f32_e32 v67, 0x3fb8aa3b, v67
	v_exp_f32_e32 v67, v67
	v_cvt_pk_bf16_f32 v89, v12, v13
	v_cvt_pk_bf16_f32 v88, v10, v11
	v_or_b32_e32 v104, 0x17400, v150
	v_mul_f32_e32 v66, v67, v66
	v_cndmask_b32_e64 v66, 0, v66, s[0:1]
	v_cvt_pk_bf16_f32 v57, v56, v57
	v_cvt_pk_bf16_f32 v56, v54, v55
	v_add_f32_dpp v67, v66, v66 quad_perm:[1,0,3,2] row_mask:0xf bank_mask:0xf bound_ctrl:1
	v_cvt_pk_bf16_f32 v54, v50, v51
	v_cvt_pk_bf16_f32 v50, v58, v59
	v_add_f32_dpp v67, v67, v67 quad_perm:[2,3,0,1] row_mask:0xf bank_mask:0xf bound_ctrl:1
	v_or_b32_e32 v58, 0x17800, v150
	v_cvt_pk_bf16_f32 v55, v52, v53
	v_add_f32_dpp v67, v67, v67 row_half_mirror row_mask:0xf bank_mask:0xf bound_ctrl:1
	v_cvt_pk_bf16_f32 v53, v64, v65
	v_cvt_pk_bf16_f32 v52, v62, v63
	v_add_f32_dpp v67, v67, v67 row_ror:8 row_mask:0xf bank_mask:0xf bound_ctrl:1
	v_mov_b32_e32 v68, v67
	s_nop 1
	v_permlane16_swap_b32_e32 v67, v68
	v_add_f32_e32 v67, v67, v68
	v_mov_b32_e32 v68, v67
	s_nop 1
	v_permlane32_swap_b32_e32 v67, v68
	v_add_f32_e32 v67, v67, v68
	v_rcp_f32_e32 v67, v67
	v_cvt_pk_bf16_f32 v51, v60, v61
	v_cvt_pk_bf16_f32 v25, v24, v25
	v_cvt_pk_bf16_f32 v24, v22, v23
	v_mul_f32_e32 v66, v66, v67
	v_cndmask_b32_e32 v67, v131, v130, vcc
	v_mul_f32_e32 v66, v67, v66
	ds_write_b32 v173, v66 offset:768
	s_waitcnt lgkmcnt(0)
	v_or_b32_e32 v66, 0x16c00, v150
	ds_read_b128 v[82:85], v66
	ds_read_b128 v[92:95], v2
	v_or_b32_e32 v2, 0x17c00, v150
	ds_read_b128 v[96:99], v2
	ds_read_b128 v[100:103], v100
	s_waitcnt lgkmcnt(3)
	v_mfma_f32_32x32x16_bf16 v[66:81], v[6:9], v[82:85], 0
	ds_read_b128 v[104:107], v104
	ds_read_b32 v87, v135 offset:34816
	v_cvt_pk_bf16_f32 v23, v20, v21
	v_cvt_pk_bf16_f32 v22, v18, v19
	v_cvt_pk_bf16_f32 v119, v32, v33
	v_cvt_pk_bf16_f32 v118, v30, v31
	v_cvt_pk_bf16_f32 v117, v28, v29
	s_waitcnt lgkmcnt(3)
	v_mfma_f32_32x32x16_bf16 v[2:17], v[6:9], v[96:99], 0
	v_cvt_pk_bf16_f32 v116, v26, v27
	v_cvt_pk_bf16_f32 v41, v40, v41
	v_cvt_pk_bf16_f32 v40, v38, v39
	v_cvt_pk_bf16_f32 v39, v36, v37
	v_cvt_pk_bf16_f32 v38, v34, v35
	v_cvt_pk_bf16_f32 v37, v48, v49
	v_cvt_pk_bf16_f32 v36, v46, v47
	v_mfma_f32_32x32x16_bf16 v[66:81], v[88:91], v[92:95], v[66:81]
	v_cvt_pk_bf16_f32 v35, v44, v45
	v_cvt_pk_bf16_f32 v34, v42, v43
	s_waitcnt lgkmcnt(2)
	v_mfma_f32_32x32x16_bf16 v[2:17], v[88:91], v[100:103], v[2:17]
	ds_read_b128 v[88:91], v58
	v_or_b32_e32 v58, 0x18400, v150
	ds_read_b128 v[108:111], v58
	s_waitcnt lgkmcnt(3)
	v_mfma_f32_32x32x16_bf16 v[66:81], v[54:57], v[104:107], v[66:81]
	s_waitcnt lgkmcnt(0)
	v_mfma_f32_32x32x16_bf16 v[2:17], v[54:57], v[108:111], v[2:17]
	v_or_b32_e32 v54, 0x18800, v150
	ds_read_b128 v[112:115], v54
	v_mfma_f32_32x32x16_bf16 v[66:81], v[50:53], v[88:91], v[66:81]
	s_waitcnt lgkmcnt(0)
	v_mfma_f32_32x32x16_bf16 v[2:17], v[50:53], v[112:115], v[2:17]
	v_mfma_f32_32x32x16_bf16 v[50:65], v[22:25], v[82:85], 0
	v_mfma_f32_32x32x16_bf16 v[18:33], v[22:25], v[96:99], 0
	v_mfma_f32_32x32x16_bf16 v[50:65], v[116:119], v[92:95], v[50:65]
	v_mfma_f32_32x32x16_bf16 v[18:33], v[116:119], v[100:103], v[18:33]
	v_mfma_f32_32x32x16_bf16 v[50:65], v[38:41], v[104:107], v[50:65]
	v_mfma_f32_32x32x16_bf16 v[18:33], v[38:41], v[108:111], v[18:33]
	ds_read_b128 v[38:41], v134 offset:896
	ds_read_b128 v[42:45], v134 offset:928
	v_mfma_f32_32x32x16_bf16 v[50:65], v[34:37], v[88:91], v[50:65]
	v_mfma_f32_32x32x16_bf16 v[18:33], v[34:37], v[112:115], v[18:33]
	ds_read_b128 v[34:37], v134 offset:960
	ds_read_b128 v[46:49], v134 offset:992
	ds_read_b128 v[82:85], v134 offset:768
	ds_read_b128 v[88:91], v134 offset:800
	ds_read_b128 v[92:95], v134 offset:832
	ds_read_b128 v[96:99], v134 offset:864
	s_waitcnt lgkmcnt(6)
	s_nop 3
	v_mul_f32_e32 v54, v42, v54
	v_mul_f32_e32 v55, v43, v55
	s_waitcnt lgkmcnt(4)
	v_mul_f32_e32 v62, v46, v62
	v_mul_f32_e32 v63, v47, v63
	v_mul_f32_e32 v56, v44, v56
	v_mul_f32_e32 v57, v45, v57
	v_mul_f32_e32 v64, v48, v64
	v_mul_f32_e32 v65, v49, v65
	v_mul_f32_e32 v52, v40, v52
	v_mul_f32_e32 v53, v41, v53
	v_mul_f32_e32 v60, v36, v60
	v_mul_f32_e32 v61, v37, v61
	v_mul_f32_e32 v58, v34, v58
	v_mul_f32_e32 v59, v35, v59
	v_mul_f32_e32 v50, v38, v50
	v_mul_f32_e32 v51, v39, v51
	v_mul_f32_e32 v22, v42, v22
	v_mul_f32_e32 v23, v43, v23
	v_mul_f32_e32 v30, v46, v30
	v_mul_f32_e32 v31, v47, v31
	v_mul_f32_e32 v24, v44, v24
	v_mul_f32_e32 v25, v45, v25
	v_mul_f32_e32 v32, v48, v32
	v_mul_f32_e32 v33, v49, v33
	v_mul_f32_e32 v20, v40, v20
	v_mul_f32_e32 v21, v41, v21
	v_mul_f32_e32 v28, v36, v28
	v_mul_f32_e32 v29, v37, v29
	v_mul_f32_e32 v26, v34, v26
	v_mul_f32_e32 v27, v35, v27
	v_mul_f32_e32 v18, v38, v18
	v_mul_f32_e32 v19, v39, v19
	s_waitcnt lgkmcnt(1)
	v_fmac_f32_e32 v58, v92, v74
	v_fmac_f32_e32 v59, v93, v75
	v_fmac_f32_e32 v60, v94, v76
	v_fmac_f32_e32 v61, v95, v77
	v_fmac_f32_e32 v52, v84, v68
	v_fmac_f32_e32 v53, v85, v69
	s_waitcnt lgkmcnt(0)
	v_fmac_f32_e32 v64, v98, v80
	v_fmac_f32_e32 v65, v99, v81
	v_fmac_f32_e32 v56, v90, v72
	v_fmac_f32_e32 v57, v91, v73
	v_fmac_f32_e32 v62, v96, v78
	v_fmac_f32_e32 v63, v97, v79
	v_fmac_f32_e32 v54, v88, v70
	v_fmac_f32_e32 v55, v89, v71
	v_fmac_f32_e32 v50, v82, v66
	v_fmac_f32_e32 v51, v83, v67
	v_fma_f32 v10, v92, v10, v26
	v_fma_f32 v11, v93, v11, v27
	v_fma_f32 v12, v94, v12, v28
	v_fma_f32 v13, v95, v13, v29
	v_fma_f32 v4, v84, v4, v20
	v_fma_f32 v5, v85, v5, v21
	v_fma_f32 v16, v98, v16, v32
	v_fma_f32 v17, v99, v17, v33
	v_fma_f32 v8, v90, v8, v24
	v_fma_f32 v9, v91, v9, v25
	v_fma_f32 v14, v96, v14, v30
	v_fma_f32 v15, v97, v15, v31
	v_fma_f32 v6, v88, v6, v22
	v_fma_f32 v7, v89, v7, v23
	v_fma_f32 v2, v82, v2, v18
	v_fma_f32 v3, v83, v3, v19
	v_add_f32_e32 v54, v54, v62
	v_add_f32_e32 v55, v55, v63
	v_add_f32_e32 v56, v56, v64
	v_add_f32_e32 v57, v57, v65
	v_add_f32_e32 v52, v52, v60
	v_add_f32_e32 v53, v53, v61
	v_add_f32_e32 v50, v50, v58
	v_add_f32_e32 v51, v51, v59
	v_add_f32_e32 v6, v6, v14
	v_add_f32_e32 v7, v7, v15
	v_add_f32_e32 v8, v8, v16
	v_add_f32_e32 v9, v9, v17
	v_add_f32_e32 v4, v4, v12
	v_add_f32_e32 v5, v5, v13
	v_add_f32_e32 v2, v2, v10
	v_add_f32_e32 v3, v3, v11
	v_add_f32_e32 v52, v52, v56
	v_add_f32_e32 v53, v53, v57
	v_add_f32_e32 v50, v50, v54
	v_add_f32_e32 v51, v51, v55
	v_add_f32_e32 v4, v4, v8
	v_add_f32_e32 v5, v5, v9
	v_add_f32_e32 v2, v2, v6
	v_add_f32_e32 v3, v3, v7
	v_add_f32_e32 v50, v50, v51
	v_add_f32_e32 v51, v52, v53
	v_add_f32_e32 v2, v2, v3
	v_add_f32_e32 v3, v4, v5
	v_add_f32_e32 v50, v50, v51
	v_add_f32_e32 v2, v2, v3
	v_mov_b32_e32 v3, v50
	v_mov_b32_e32 v4, v2
	s_nop 0
	v_permlane32_swap_b32_e32 v50, v3
	v_permlane32_swap_b32_e32 v2, v4
	v_add_f32_e32 v3, v50, v3
	v_add_f32_e32 v2, v2, v4
	v_cndmask_b32_e32 v2, v2, v3, vcc
	v_add_f32_e32 v3, v87, v2
	v_cmp_eq_u32_e32 vcc, 0, v1
	s_nop 0
	v_mov_b32_dpp v2, v3 quad_perm:[1,0,3,2] row_mask:0xf bank_mask:0xf bound_ctrl:1
	v_max_f32_e32 v2, v2, v2
	v_max_f32_e32 v2, v3, v2
	s_nop 1
	v_mov_b32_dpp v4, v2 quad_perm:[2,3,0,1] row_mask:0xf bank_mask:0xf bound_ctrl:1
	v_max_f32_e32 v4, v4, v4
	v_max_f32_e32 v2, v2, v4
	s_nop 1
	v_mov_b32_dpp v4, v2 row_half_mirror row_mask:0xf bank_mask:0xf bound_ctrl:1
	v_max_f32_e32 v4, v4, v4
	v_max_f32_e32 v2, v2, v4
	s_nop 1
	v_mov_b32_dpp v4, v2 row_ror:8 row_mask:0xf bank_mask:0xf bound_ctrl:1
	v_max_f32_e32 v4, v4, v4
	v_max_f32_e32 v2, v2, v4
	v_mov_b32_e32 v4, v2
	s_nop 1
	v_permlane16_swap_b32_e32 v2, v4
	v_max_f32_e32 v4, v4, v4
	v_max_f32_e32 v2, v2, v2
	v_max_f32_e32 v2, v2, v4
	v_mov_b32_e32 v4, v2
	s_nop 1
	v_permlane32_swap_b32_e32 v2, v4
	v_max_f32_e32 v4, v4, v4
	v_max_f32_e32 v2, v2, v2
	v_max_f32_e32 v2, v2, v4
	v_sub_f32_e32 v4, v3, v2
	v_mul_f32_e32 v4, 0x3fb8aa3b, v4
	v_exp_f32_e32 v4, v4
	s_nop 1
	v_add_f32_dpp v4, v4, v4 quad_perm:[1,0,3,2] row_mask:0xf bank_mask:0xf bound_ctrl:1
	s_nop 1
	v_add_f32_dpp v4, v4, v4 quad_perm:[2,3,0,1] row_mask:0xf bank_mask:0xf bound_ctrl:1
	s_nop 1
	v_add_f32_dpp v4, v4, v4 row_half_mirror row_mask:0xf bank_mask:0xf bound_ctrl:1
	s_nop 1
	v_add_f32_dpp v4, v4, v4 row_ror:8 row_mask:0xf bank_mask:0xf bound_ctrl:1
	v_mov_b32_e32 v5, v4
	s_nop 1
	v_permlane16_swap_b32_e32 v4, v5
	v_add_f32_e32 v4, v4, v5
	v_and_or_b32 v5, s3, 63, v86
	v_lshlrev_b32_e32 v5, 2, v5
	ds_bpermute_b32 v3, v5, v3
	v_mov_b32_e32 v5, v4
	s_nop 1
	v_permlane32_swap_b32_e32 v4, v5
	s_and_saveexec_b64 s[4:5], vcc
	s_cbranch_execz .LBB1_12
	v_add_f32_e32 v1, v4, v5
	s_mov_b32 s0, 0x800000
	v_cmp_gt_f32_e32 vcc, s0, v1
	s_mov_b32 s0, 0x3f317217
	s_nop 0
	v_cndmask_b32_e64 v4, 0, 32, vcc
	v_ldexp_f32 v1, v1, v4
	v_log_f32_e32 v1, v1
	s_nop 0
	v_mul_f32_e32 v4, 0x3f317217, v1
	v_fma_f32 v4, v1, s0, -v4
	v_fmamk_f32 v4, v1, 0x3377d1cf, v4
	s_mov_b32 s0, 0x7f800000
	v_fmac_f32_e32 v4, 0x3f317217, v1
	v_cmp_lt_f32_e64 s[0:1], |v1|, s0
	s_nop 1
	v_cndmask_b32_e64 v1, v1, v4, s[0:1]
	v_mov_b32_e32 v4, 0x41b17218
	v_cndmask_b32_e32 v4, 0, v4, vcc
	v_sub_f32_e32 v1, v1, v4
	v_add_f32_e32 v1, v2, v1
	s_waitcnt lgkmcnt(0)
	v_sub_f32_e32 v1, v1, v3
	ds_write_b32 v172, v1

	.amdhsa_kernel _Z9fast_mainILb0EEvPKiS1_S1_PKfPKcS3_PfS6_PiPyS6_
		.amdhsa_group_segment_fixed_size 150528
		.amdhsa_private_segment_fixed_size 0
		.amdhsa_kernarg_size 88
		.amdhsa_user_sgpr_count 2
		.amdhsa_user_sgpr_dispatch_ptr 0
		.amdhsa_user_sgpr_queue_ptr 0
		.amdhsa_user_sgpr_kernarg_segment_ptr 1
		.amdhsa_user_sgpr_dispatch_id 0
		.amdhsa_user_sgpr_kernarg_preload_length 0
		.amdhsa_user_sgpr_kernarg_preload_offset 0
		.amdhsa_user_sgpr_private_segment_size 0
		.amdhsa_uses_dynamic_stack 0
		.amdhsa_enable_private_segment 0
		.amdhsa_system_sgpr_workgroup_id_x 1
		.amdhsa_system_sgpr_workgroup_id_y 0
		.amdhsa_system_sgpr_workgroup_id_z 0
		.amdhsa_system_sgpr_workgroup_info 0
		.amdhsa_system_vgpr_workitem_id 0
		.amdhsa_next_free_vgpr 212
		.amdhsa_next_free_sgpr 96
		.amdhsa_accum_offset 212
		.amdhsa_reserve_vcc 1
		.amdhsa_float_round_mode_32 0
		.amdhsa_float_round_mode_16_64 0
		.amdhsa_float_denorm_mode_32 3
		.amdhsa_float_denorm_mode_16_64 3
		.amdhsa_dx10_clamp 1
		.amdhsa_ieee_mode 1
		.amdhsa_fp16_overflow 0
		.amdhsa_tg_split 0
		.amdhsa_exception_fp_ieee_invalid_op 0
		.amdhsa_exception_fp_denorm_src 0
		.amdhsa_exception_fp_ieee_div_zero 0
		.amdhsa_exception_fp_ieee_overflow 0
		.amdhsa_exception_fp_ieee_underflow 0
		.amdhsa_exception_fp_ieee_inexact 0
		.amdhsa_exception_int_div_zero 0
	.end_amdhsa_kernel
	.text
.Lfunc_end1:
	.size	_Z9fast_mainILb0EEvPKiS1_S1_PKfPKcS3_PfS6_PiPyS6_, .Lfunc_end1-_Z9fast_mainILb0EEvPKiS1_S1_PKfPKcS3_PfS6_PiPyS6_
	.set _Z9fast_mainILb0EEvPKiS1_S1_PKfPKcS3_PfS6_PiPyS6_.num_vgpr, 212
	.set _Z9fast_mainILb0EEvPKiS1_S1_PKfPKcS3_PfS6_PiPyS6_.num_agpr, 0
	.set _Z9fast_mainILb0EEvPKiS1_S1_PKfPKcS3_PfS6_PiPyS6_.numbered_sgpr, 16
	.set _Z9fast_mainILb0EEvPKiS1_S1_PKfPKcS3_PfS6_PiPyS6_.num_named_barrier, 0
	.set _Z9fast_mainILb0EEvPKiS1_S1_PKfPKcS3_PfS6_PiPyS6_.private_seg_size, 0
	.set _Z9fast_mainILb0EEvPKiS1_S1_PKfPKcS3_PfS6_PiPyS6_.uses_vcc, 1
	.set _Z9fast_mainILb0EEvPKiS1_S1_PKfPKcS3_PfS6_PiPyS6_.uses_flat_scratch, 0
	.set _Z9fast_mainILb0EEvPKiS1_S1_PKfPKcS3_PfS6_PiPyS6_.has_dyn_sized_stack, 0
	.set _Z9fast_mainILb0EEvPKiS1_S1_PKfPKcS3_PfS6_PiPyS6_.has_recursion, 0
	.set _Z9fast_mainILb0EEvPKiS1_S1_PKfPKcS3_PfS6_PiPyS6_.has_indirect_call, 0
